# final_d with at most 32 tile row loads in flight per wave in the barrier-hosted conversion
# speedup vs baseline: 1.0087x; 1.0087x over previous
.Lhw_go_s0_0:
	s_add_u32 s100, s82, s69
	s_addc_u32 s101, s83, 0
	v_readlane_b32 s82, v239, 44
	v_readlane_b32 s83, v239, 45
	s_add_u32 s82, s82, s98
	s_addc_u32 s83, s83, 0
	global_load_dword v34, v178, s[100:101] nt
	s_add_u32 s100, s100, s89
	s_addc_u32 s101, s101, 0
	global_load_dword v35, v178, s[100:101] nt
	s_add_u32 s100, s100, s89
	s_addc_u32 s101, s101, 0
	global_load_dword v36, v178, s[100:101] nt
	s_add_u32 s100, s100, s89
	s_addc_u32 s101, s101, 0
	global_load_dword v37, v178, s[100:101] nt
	s_add_u32 s100, s100, s89
	s_addc_u32 s101, s101, 0
	global_load_dword v38, v178, s[100:101] nt
	s_add_u32 s100, s100, s89
	s_addc_u32 s101, s101, 0
	global_load_dword v39, v178, s[100:101] nt
	s_add_u32 s100, s100, s89
	s_addc_u32 s101, s101, 0
	global_load_dword v40, v178, s[100:101] nt
	s_add_u32 s100, s100, s89
	s_addc_u32 s101, s101, 0
	global_load_dword v41, v178, s[100:101] nt
	s_add_u32 s100, s100, s89
	s_addc_u32 s101, s101, 0
	global_load_dword v42, v178, s[100:101] nt
	s_add_u32 s100, s100, s89
	s_addc_u32 s101, s101, 0
	global_load_dword v43, v178, s[100:101] nt
	s_add_u32 s100, s100, s89
	s_addc_u32 s101, s101, 0
	global_load_dword v44, v178, s[100:101] nt
	s_add_u32 s100, s100, s89
	s_addc_u32 s101, s101, 0
	global_load_dword v45, v178, s[100:101] nt
	s_add_u32 s100, s100, s89
	s_addc_u32 s101, s101, 0
	global_load_dword v46, v178, s[100:101] nt
	s_add_u32 s100, s100, s89
	s_addc_u32 s101, s101, 0
	global_load_dword v47, v178, s[100:101] nt
	s_add_u32 s100, s100, s89
	s_addc_u32 s101, s101, 0
	global_load_dword v48, v178, s[100:101] nt
	s_add_u32 s100, s100, s89
	s_addc_u32 s101, s101, 0
	global_load_dword v49, v178, s[100:101] nt
	s_add_u32 s100, s100, s89
	s_addc_u32 s101, s101, 0
	global_load_dword v50, v178, s[100:101] nt
	s_add_u32 s100, s100, s89
	s_addc_u32 s101, s101, 0
	global_load_dword v51, v178, s[100:101] nt
	s_add_u32 s100, s100, s89
	s_addc_u32 s101, s101, 0
	global_load_dword v52, v178, s[100:101] nt
	s_add_u32 s100, s100, s89
	s_addc_u32 s101, s101, 0
	global_load_dword v53, v178, s[100:101] nt
	s_add_u32 s100, s100, s89
	s_addc_u32 s101, s101, 0
	global_load_dword v54, v178, s[100:101] nt
	s_add_u32 s100, s100, s89
	s_addc_u32 s101, s101, 0
	global_load_dword v55, v178, s[100:101] nt
	s_add_u32 s100, s100, s89
	s_addc_u32 s101, s101, 0
	global_load_dword v56, v178, s[100:101] nt
	s_add_u32 s100, s100, s89
	s_addc_u32 s101, s101, 0
	global_load_dword v57, v178, s[100:101] nt
	s_add_u32 s100, s100, s89
	s_addc_u32 s101, s101, 0
	global_load_dword v58, v178, s[100:101] nt
	s_add_u32 s100, s100, s89
	s_addc_u32 s101, s101, 0
	global_load_dword v59, v178, s[100:101] nt
	s_add_u32 s100, s100, s89
	s_addc_u32 s101, s101, 0
	global_load_dword v60, v178, s[100:101] nt
	s_add_u32 s100, s100, s89
	s_addc_u32 s101, s101, 0
	global_load_dword v61, v178, s[100:101] nt
	s_add_u32 s100, s100, s89
	s_addc_u32 s101, s101, 0
	global_load_dword v62, v178, s[100:101] nt
	s_add_u32 s100, s100, s89
	s_addc_u32 s101, s101, 0
	global_load_dword v63, v178, s[100:101] nt
	s_add_u32 s100, s100, s89
	s_addc_u32 s101, s101, 0
	global_load_dword v64, v178, s[100:101] nt
	s_add_u32 s100, s100, s89
	s_addc_u32 s101, s101, 0
	global_load_dword v65, v178, s[100:101] nt
	s_add_u32 s100, s100, s89
	s_addc_u32 s101, s101, 0
	s_waitcnt vmcnt(16)
	v_mul_f32_e32 v34, 0x42000000, v34
	v_mul_f32_e32 v35, 0x42000000, v35
	v_mul_f32_e32 v36, 0x42000000, v36
	v_mul_f32_e32 v37, 0x42000000, v37
	v_mul_f32_e32 v38, 0x42000000, v38
	v_mul_f32_e32 v39, 0x42000000, v39
	v_mul_f32_e32 v40, 0x42000000, v40
	v_mul_f32_e32 v41, 0x42000000, v41
	v_mul_f32_e32 v42, 0x42000000, v42
	v_mul_f32_e32 v43, 0x42000000, v43
	v_mul_f32_e32 v44, 0x42000000, v44
	v_mul_f32_e32 v45, 0x42000000, v45
	v_mul_f32_e32 v46, 0x42000000, v46
	v_mul_f32_e32 v47, 0x42000000, v47
	v_mul_f32_e32 v48, 0x42000000, v48
	v_mul_f32_e32 v49, 0x42000000, v49
	v_cvt_pk_fp8_f32 v154, v34, v35
	v_cvt_pk_fp8_f32 v155, v38, v39
	v_cvt_pk_fp8_f32 v156, v42, v43
	v_cvt_pk_fp8_f32 v157, v46, v47
	v_cvt_pk_fp8_f32 v154, v36, v37 op_sel:[0,0,1]
	v_cvt_pk_fp8_f32 v155, v40, v41 op_sel:[0,0,1]
	v_cvt_pk_fp8_f32 v156, v44, v45 op_sel:[0,0,1]
	v_cvt_pk_fp8_f32 v157, v48, v49 op_sel:[0,0,1]
	global_load_dword v66, v178, s[100:101] nt
	s_add_u32 s100, s100, s89
	s_addc_u32 s101, s101, 0
	global_load_dword v67, v178, s[100:101] nt
	s_add_u32 s100, s100, s89
	s_addc_u32 s101, s101, 0
	global_load_dword v68, v178, s[100:101] nt
	s_add_u32 s100, s100, s89
	s_addc_u32 s101, s101, 0
	global_load_dword v69, v178, s[100:101] nt
	s_add_u32 s100, s100, s89
	s_addc_u32 s101, s101, 0
	global_load_dword v70, v178, s[100:101] nt
	s_add_u32 s100, s100, s89
	s_addc_u32 s101, s101, 0
	global_load_dword v71, v178, s[100:101] nt
	s_add_u32 s100, s100, s89
	s_addc_u32 s101, s101, 0
	global_load_dword v72, v178, s[100:101] nt
	s_add_u32 s100, s100, s89
	s_addc_u32 s101, s101, 0
	global_load_dword v73, v178, s[100:101] nt
	s_add_u32 s100, s100, s89
	s_addc_u32 s101, s101, 0
	global_load_dword v74, v178, s[100:101] nt
	s_add_u32 s100, s100, s89
	s_addc_u32 s101, s101, 0
	global_load_dword v75, v178, s[100:101] nt
	s_add_u32 s100, s100, s89
	s_addc_u32 s101, s101, 0
	global_load_dword v76, v178, s[100:101] nt
	s_add_u32 s100, s100, s89
	s_addc_u32 s101, s101, 0
	global_load_dword v77, v178, s[100:101] nt
	s_add_u32 s100, s100, s89
	s_addc_u32 s101, s101, 0
	global_load_dword v78, v178, s[100:101] nt
	s_add_u32 s100, s100, s89
	s_addc_u32 s101, s101, 0
	global_load_dword v79, v178, s[100:101] nt
	s_add_u32 s100, s100, s89
	s_addc_u32 s101, s101, 0
	global_load_dword v80, v178, s[100:101] nt
	s_add_u32 s100, s100, s89
	s_addc_u32 s101, s101, 0
	global_load_dword v81, v178, s[100:101] nt
	s_add_u32 s100, s100, s89
	s_addc_u32 s101, s101, 0
	s_waitcnt vmcnt(16)
	v_mul_f32_e32 v50, 0x42000000, v50
	v_mul_f32_e32 v51, 0x42000000, v51
	v_mul_f32_e32 v52, 0x42000000, v52
	v_mul_f32_e32 v53, 0x42000000, v53
	v_mul_f32_e32 v54, 0x42000000, v54
	v_mul_f32_e32 v55, 0x42000000, v55
	v_mul_f32_e32 v56, 0x42000000, v56
	v_mul_f32_e32 v57, 0x42000000, v57
	v_mul_f32_e32 v58, 0x42000000, v58
	v_mul_f32_e32 v59, 0x42000000, v59
	v_mul_f32_e32 v60, 0x42000000, v60
	v_mul_f32_e32 v61, 0x42000000, v61
	v_mul_f32_e32 v62, 0x42000000, v62
	v_mul_f32_e32 v63, 0x42000000, v63
	v_mul_f32_e32 v64, 0x42000000, v64
	v_mul_f32_e32 v65, 0x42000000, v65
	v_cvt_pk_fp8_f32 v158, v50, v51
	v_cvt_pk_fp8_f32 v159, v54, v55
	v_cvt_pk_fp8_f32 v160, v58, v59
	v_cvt_pk_fp8_f32 v161, v62, v63
	v_cvt_pk_fp8_f32 v158, v52, v53 op_sel:[0,0,1]
	v_cvt_pk_fp8_f32 v159, v56, v57 op_sel:[0,0,1]
	v_cvt_pk_fp8_f32 v160, v60, v61 op_sel:[0,0,1]
	v_cvt_pk_fp8_f32 v161, v64, v65 op_sel:[0,0,1]
	global_load_dword v82, v178, s[100:101] nt
	s_add_u32 s100, s100, s89
	s_addc_u32 s101, s101, 0
	global_load_dword v83, v178, s[100:101] nt
	s_add_u32 s100, s100, s89
	s_addc_u32 s101, s101, 0
	global_load_dword v84, v178, s[100:101] nt
	s_add_u32 s100, s100, s89
	s_addc_u32 s101, s101, 0
	global_load_dword v85, v178, s[100:101] nt
	s_add_u32 s100, s100, s89
	s_addc_u32 s101, s101, 0
	global_load_dword v86, v178, s[100:101] nt
	s_add_u32 s100, s100, s89
	s_addc_u32 s101, s101, 0
	global_load_dword v87, v178, s[100:101] nt
	s_add_u32 s100, s100, s89
	s_addc_u32 s101, s101, 0
	global_load_dword v88, v178, s[100:101] nt
	s_add_u32 s100, s100, s89
	s_addc_u32 s101, s101, 0
	global_load_dword v89, v178, s[100:101] nt
	s_add_u32 s100, s100, s89
	s_addc_u32 s101, s101, 0
	global_load_dword v90, v178, s[100:101] nt
	s_add_u32 s100, s100, s89
	s_addc_u32 s101, s101, 0
	global_load_dword v91, v178, s[100:101] nt
	s_add_u32 s100, s100, s89
	s_addc_u32 s101, s101, 0
	global_load_dword v92, v178, s[100:101] nt
	s_add_u32 s100, s100, s89
	s_addc_u32 s101, s101, 0
	global_load_dword v93, v178, s[100:101] nt
	s_add_u32 s100, s100, s89
	s_addc_u32 s101, s101, 0
	global_load_dword v94, v178, s[100:101] nt
	s_add_u32 s100, s100, s89
	s_addc_u32 s101, s101, 0
	global_load_dword v95, v178, s[100:101] nt
	s_add_u32 s100, s100, s89
	s_addc_u32 s101, s101, 0
	global_load_dword v96, v178, s[100:101] nt
	s_add_u32 s100, s100, s89
	s_addc_u32 s101, s101, 0
	global_load_dword v97, v178, s[100:101] nt
	s_add_u32 s100, s100, s89
	s_addc_u32 s101, s101, 0
	s_waitcnt vmcnt(16)
	v_mul_f32_e32 v66, 0x42000000, v66
	v_mul_f32_e32 v67, 0x42000000, v67
	v_mul_f32_e32 v68, 0x42000000, v68
	v_mul_f32_e32 v69, 0x42000000, v69
	v_mul_f32_e32 v70, 0x42000000, v70
	v_mul_f32_e32 v71, 0x42000000, v71
	v_mul_f32_e32 v72, 0x42000000, v72
	v_mul_f32_e32 v73, 0x42000000, v73
	v_mul_f32_e32 v74, 0x42000000, v74
	v_mul_f32_e32 v75, 0x42000000, v75
	v_mul_f32_e32 v76, 0x42000000, v76
	v_mul_f32_e32 v77, 0x42000000, v77
	v_mul_f32_e32 v78, 0x42000000, v78
	v_mul_f32_e32 v79, 0x42000000, v79
	v_mul_f32_e32 v80, 0x42000000, v80
	v_mul_f32_e32 v81, 0x42000000, v81
	v_cvt_pk_fp8_f32 v162, v66, v67
	v_cvt_pk_fp8_f32 v163, v70, v71
	v_cvt_pk_fp8_f32 v164, v74, v75
	v_cvt_pk_fp8_f32 v165, v78, v79
	v_cvt_pk_fp8_f32 v162, v68, v69 op_sel:[0,0,1]
	v_cvt_pk_fp8_f32 v163, v72, v73 op_sel:[0,0,1]
	v_cvt_pk_fp8_f32 v164, v76, v77 op_sel:[0,0,1]
	v_cvt_pk_fp8_f32 v165, v80, v81 op_sel:[0,0,1]
	s_waitcnt vmcnt(0)
	v_mul_f32_e32 v82, 0x42000000, v82
	v_mul_f32_e32 v83, 0x42000000, v83
	v_mul_f32_e32 v84, 0x42000000, v84
	v_mul_f32_e32 v85, 0x42000000, v85
	v_mul_f32_e32 v86, 0x42000000, v86
	v_mul_f32_e32 v87, 0x42000000, v87
	v_mul_f32_e32 v88, 0x42000000, v88
	v_mul_f32_e32 v89, 0x42000000, v89
	v_mul_f32_e32 v90, 0x42000000, v90
	v_mul_f32_e32 v91, 0x42000000, v91
	v_mul_f32_e32 v92, 0x42000000, v92
	v_mul_f32_e32 v93, 0x42000000, v93
	v_mul_f32_e32 v94, 0x42000000, v94
	v_mul_f32_e32 v95, 0x42000000, v95
	v_mul_f32_e32 v96, 0x42000000, v96
	v_mul_f32_e32 v97, 0x42000000, v97
	v_cvt_pk_fp8_f32 v166, v82, v83
	v_cvt_pk_fp8_f32 v167, v86, v87
	v_cvt_pk_fp8_f32 v168, v90, v91
	v_cvt_pk_fp8_f32 v169, v94, v95
	v_cvt_pk_fp8_f32 v166, v84, v85 op_sel:[0,0,1]
	v_cvt_pk_fp8_f32 v167, v88, v89 op_sel:[0,0,1]
	v_cvt_pk_fp8_f32 v168, v92, v93 op_sel:[0,0,1]
	v_cvt_pk_fp8_f32 v169, v96, v97 op_sel:[0,0,1]
	s_mov_b32 vcc_lo, 0xaaaaaaaa
	s_mov_b32 vcc_hi, 0xaaaaaaaa
	s_nop 1
	v_cndmask_b32_dpp v170, v154, v158, vcc quad_perm:[1,0,3,2] row_mask:0xf bank_mask:0xf
	v_cndmask_b32_dpp v174, v162, v166, vcc quad_perm:[1,0,3,2] row_mask:0xf bank_mask:0xf
	v_cndmask_b32_dpp v171, v155, v159, vcc quad_perm:[1,0,3,2] row_mask:0xf bank_mask:0xf
	v_cndmask_b32_dpp v175, v163, v167, vcc quad_perm:[1,0,3,2] row_mask:0xf bank_mask:0xf
	v_cndmask_b32_dpp v172, v156, v160, vcc quad_perm:[1,0,3,2] row_mask:0xf bank_mask:0xf
	v_cndmask_b32_dpp v176, v164, v168, vcc quad_perm:[1,0,3,2] row_mask:0xf bank_mask:0xf
	v_cndmask_b32_dpp v173, v157, v161, vcc quad_perm:[1,0,3,2] row_mask:0xf bank_mask:0xf
	v_cndmask_b32_dpp v177, v165, v169, vcc quad_perm:[1,0,3,2] row_mask:0xf bank_mask:0xf
	s_mov_b32 vcc_lo, 0x55555555
	s_mov_b32 vcc_hi, 0x55555555
	s_nop 1
	v_cndmask_b32_dpp v154, v158, v154, vcc quad_perm:[1,0,3,2] row_mask:0xf bank_mask:0xf
	v_cndmask_b32_dpp v162, v166, v162, vcc quad_perm:[1,0,3,2] row_mask:0xf bank_mask:0xf
	v_cndmask_b32_dpp v155, v159, v155, vcc quad_perm:[1,0,3,2] row_mask:0xf bank_mask:0xf
	v_cndmask_b32_dpp v163, v167, v163, vcc quad_perm:[1,0,3,2] row_mask:0xf bank_mask:0xf
	v_cndmask_b32_dpp v156, v160, v156, vcc quad_perm:[1,0,3,2] row_mask:0xf bank_mask:0xf
	v_cndmask_b32_dpp v164, v168, v164, vcc quad_perm:[1,0,3,2] row_mask:0xf bank_mask:0xf
	v_cndmask_b32_dpp v157, v161, v157, vcc quad_perm:[1,0,3,2] row_mask:0xf bank_mask:0xf
	v_cndmask_b32_dpp v165, v169, v165, vcc quad_perm:[1,0,3,2] row_mask:0xf bank_mask:0xf
	s_mov_b32 vcc_lo, 0xcccccccc
	s_mov_b32 vcc_hi, 0xcccccccc
	s_nop 1
	v_cndmask_b32_dpp v158, v154, v162, vcc quad_perm:[2,3,0,1] row_mask:0xf bank_mask:0xf
	v_cndmask_b32_dpp v166, v170, v174, vcc quad_perm:[2,3,0,1] row_mask:0xf bank_mask:0xf
	v_cndmask_b32_dpp v159, v155, v163, vcc quad_perm:[2,3,0,1] row_mask:0xf bank_mask:0xf
	v_cndmask_b32_dpp v167, v171, v175, vcc quad_perm:[2,3,0,1] row_mask:0xf bank_mask:0xf
	v_cndmask_b32_dpp v160, v156, v164, vcc quad_perm:[2,3,0,1] row_mask:0xf bank_mask:0xf
	v_cndmask_b32_dpp v168, v172, v176, vcc quad_perm:[2,3,0,1] row_mask:0xf bank_mask:0xf
	v_cndmask_b32_dpp v161, v157, v165, vcc quad_perm:[2,3,0,1] row_mask:0xf bank_mask:0xf
	v_cndmask_b32_dpp v169, v173, v177, vcc quad_perm:[2,3,0,1] row_mask:0xf bank_mask:0xf
	s_mov_b32 vcc_lo, 0x33333333
	s_mov_b32 vcc_hi, 0x33333333
	s_nop 1
	v_cndmask_b32_dpp v154, v162, v154, vcc quad_perm:[2,3,0,1] row_mask:0xf bank_mask:0xf
	v_cndmask_b32_dpp v170, v174, v170, vcc quad_perm:[2,3,0,1] row_mask:0xf bank_mask:0xf
	v_cndmask_b32_dpp v155, v163, v155, vcc quad_perm:[2,3,0,1] row_mask:0xf bank_mask:0xf
	v_cndmask_b32_dpp v171, v175, v171, vcc quad_perm:[2,3,0,1] row_mask:0xf bank_mask:0xf
	v_cndmask_b32_dpp v156, v164, v156, vcc quad_perm:[2,3,0,1] row_mask:0xf bank_mask:0xf
	v_cndmask_b32_dpp v172, v176, v172, vcc quad_perm:[2,3,0,1] row_mask:0xf bank_mask:0xf
	v_cndmask_b32_dpp v157, v165, v157, vcc quad_perm:[2,3,0,1] row_mask:0xf bank_mask:0xf
	v_cndmask_b32_dpp v173, v177, v173, vcc quad_perm:[2,3,0,1] row_mask:0xf bank_mask:0xf
	global_store_dwordx4 v179, v[154:157], s[82:83] nt
	global_store_dwordx4 v180, v[170:173], s[82:83] nt
	global_store_dwordx4 v181, v[158:161], s[82:83] nt
	global_store_dwordx4 v190, v[166:169], s[82:83] nt
	v_readlane_b32 s2, v239, 0
	s_lshr_b32 s2, s2, 6
	s_add_i32 s2, s2, 6
	s_cmp_gt_u32 s2, 13
	s_cbranch_scc1 .Lhw_seam0_done
	s_add_i32 s2, s2, 0
	s_mul_i32 s2, s2, s74
	v_readlane_b32 s9, v239, 23
	s_lshr_b32 s9, s9, 3
	s_add_i32 s2, s2, s9
	s_cmp_gt_u32 s2, 24575
	s_cbranch_scc1 .Lhw_seam0_done
	v_mbcnt_lo_u32_b32 v178, -1, 0
	v_mbcnt_hi_u32_b32 v178, -1, v178
	v_and_b32_e32 v179, 60, v178
	v_lshlrev_b32_e32 v179, 10, v179
	v_and_b32_e32 v180, 3, v178
	v_lshl_or_b32 v179, v180, 4, v179
	v_add_u32_e32 v180, 0x400, v179
	v_add_u32_e32 v181, 0x800, v179
	v_add_u32_e32 v190, 0xc00, v179
	v_lshlrev_b32_e32 v178, 2, v178
	s_cmp_lt_u32 s2, 16384
	s_cbranch_scc0 .Lhw_dn_s0_1
	s_lshr_b32 s9, s2, 9
	s_bfe_u32 s32, s2, 0x40005
	s_and_b32 s53, s2, 31
	s_lshl_b32 s69, s9, 23
	s_lshl_b32 s100, s32, 19
	s_add_i32 s69, s69, s100
	s_lshl_b32 s100, s53, 8
	s_add_i32 s69, s69, s100
	s_lshl_b32 s98, s9, 11
	s_bfe_u32 s100, s53, 0x30001
	s_lshl_b32 s100, s100, 8
	s_add_i32 s98, s98, s100
	s_lshr_b32 s100, s53, 4
	s_lshl_b32 s100, s100, 7
	s_add_i32 s98, s98, s100
	s_and_b32 s100, s53, 1
	s_lshl_b32 s100, s100, 6
	s_add_i32 s98, s98, s100
	s_lshl_b32 s98, s98, 10
	s_lshl_b32 s100, s32, 6
	s_add_i32 s98, s98, s100
	s_add_i32 s98, s98, 0x2000000
	v_readlane_b32 s82, v239, 11
	v_readlane_b32 s83, v239, 12
	s_movk_i32 s89, 8192
	s_branch .Lhw_go_s0_1

.Lhw_go_s0_1:
	s_add_u32 s100, s82, s69
	s_addc_u32 s101, s83, 0
	v_readlane_b32 s82, v239, 44
	v_readlane_b32 s83, v239, 45
	s_add_u32 s82, s82, s98
	s_addc_u32 s83, s83, 0
	global_load_dword v34, v178, s[100:101] nt
	s_add_u32 s100, s100, s89
	s_addc_u32 s101, s101, 0
	global_load_dword v35, v178, s[100:101] nt
	s_add_u32 s100, s100, s89
	s_addc_u32 s101, s101, 0
	global_load_dword v36, v178, s[100:101] nt
	s_add_u32 s100, s100, s89
	s_addc_u32 s101, s101, 0
	global_load_dword v37, v178, s[100:101] nt
	s_add_u32 s100, s100, s89
	s_addc_u32 s101, s101, 0
	global_load_dword v38, v178, s[100:101] nt
	s_add_u32 s100, s100, s89
	s_addc_u32 s101, s101, 0
	global_load_dword v39, v178, s[100:101] nt
	s_add_u32 s100, s100, s89
	s_addc_u32 s101, s101, 0
	global_load_dword v40, v178, s[100:101] nt
	s_add_u32 s100, s100, s89
	s_addc_u32 s101, s101, 0
	global_load_dword v41, v178, s[100:101] nt
	s_add_u32 s100, s100, s89
	s_addc_u32 s101, s101, 0
	global_load_dword v42, v178, s[100:101] nt
	s_add_u32 s100, s100, s89
	s_addc_u32 s101, s101, 0
	global_load_dword v43, v178, s[100:101] nt
	s_add_u32 s100, s100, s89
	s_addc_u32 s101, s101, 0
	global_load_dword v44, v178, s[100:101] nt
	s_add_u32 s100, s100, s89
	s_addc_u32 s101, s101, 0
	global_load_dword v45, v178, s[100:101] nt
	s_add_u32 s100, s100, s89
	s_addc_u32 s101, s101, 0
	global_load_dword v46, v178, s[100:101] nt
	s_add_u32 s100, s100, s89
	s_addc_u32 s101, s101, 0
	global_load_dword v47, v178, s[100:101] nt
	s_add_u32 s100, s100, s89
	s_addc_u32 s101, s101, 0
	global_load_dword v48, v178, s[100:101] nt
	s_add_u32 s100, s100, s89
	s_addc_u32 s101, s101, 0
	global_load_dword v49, v178, s[100:101] nt
	s_add_u32 s100, s100, s89
	s_addc_u32 s101, s101, 0
	global_load_dword v50, v178, s[100:101] nt
	s_add_u32 s100, s100, s89
	s_addc_u32 s101, s101, 0
	global_load_dword v51, v178, s[100:101] nt
	s_add_u32 s100, s100, s89
	s_addc_u32 s101, s101, 0
	global_load_dword v52, v178, s[100:101] nt
	s_add_u32 s100, s100, s89
	s_addc_u32 s101, s101, 0
	global_load_dword v53, v178, s[100:101] nt
	s_add_u32 s100, s100, s89
	s_addc_u32 s101, s101, 0
	global_load_dword v54, v178, s[100:101] nt
	s_add_u32 s100, s100, s89
	s_addc_u32 s101, s101, 0
	global_load_dword v55, v178, s[100:101] nt
	s_add_u32 s100, s100, s89
	s_addc_u32 s101, s101, 0
	global_load_dword v56, v178, s[100:101] nt
	s_add_u32 s100, s100, s89
	s_addc_u32 s101, s101, 0
	global_load_dword v57, v178, s[100:101] nt
	s_add_u32 s100, s100, s89
	s_addc_u32 s101, s101, 0
	global_load_dword v58, v178, s[100:101] nt
	s_add_u32 s100, s100, s89
	s_addc_u32 s101, s101, 0
	global_load_dword v59, v178, s[100:101] nt
	s_add_u32 s100, s100, s89
	s_addc_u32 s101, s101, 0
	global_load_dword v60, v178, s[100:101] nt
	s_add_u32 s100, s100, s89
	s_addc_u32 s101, s101, 0
	global_load_dword v61, v178, s[100:101] nt
	s_add_u32 s100, s100, s89
	s_addc_u32 s101, s101, 0
	global_load_dword v62, v178, s[100:101] nt
	s_add_u32 s100, s100, s89
	s_addc_u32 s101, s101, 0
	global_load_dword v63, v178, s[100:101] nt
	s_add_u32 s100, s100, s89
	s_addc_u32 s101, s101, 0
	global_load_dword v64, v178, s[100:101] nt
	s_add_u32 s100, s100, s89
	s_addc_u32 s101, s101, 0
	global_load_dword v65, v178, s[100:101] nt
	s_add_u32 s100, s100, s89
	s_addc_u32 s101, s101, 0
	s_waitcnt vmcnt(16)
	v_mul_f32_e32 v34, 0x42000000, v34
	v_mul_f32_e32 v35, 0x42000000, v35
	v_mul_f32_e32 v36, 0x42000000, v36
	v_mul_f32_e32 v37, 0x42000000, v37
	v_mul_f32_e32 v38, 0x42000000, v38
	v_mul_f32_e32 v39, 0x42000000, v39
	v_mul_f32_e32 v40, 0x42000000, v40
	v_mul_f32_e32 v41, 0x42000000, v41
	v_mul_f32_e32 v42, 0x42000000, v42
	v_mul_f32_e32 v43, 0x42000000, v43
	v_mul_f32_e32 v44, 0x42000000, v44
	v_mul_f32_e32 v45, 0x42000000, v45
	v_mul_f32_e32 v46, 0x42000000, v46
	v_mul_f32_e32 v47, 0x42000000, v47
	v_mul_f32_e32 v48, 0x42000000, v48
	v_mul_f32_e32 v49, 0x42000000, v49
	v_cvt_pk_fp8_f32 v154, v34, v35
	v_cvt_pk_fp8_f32 v155, v38, v39
	v_cvt_pk_fp8_f32 v156, v42, v43
	v_cvt_pk_fp8_f32 v157, v46, v47
	v_cvt_pk_fp8_f32 v154, v36, v37 op_sel:[0,0,1]
	v_cvt_pk_fp8_f32 v155, v40, v41 op_sel:[0,0,1]
	v_cvt_pk_fp8_f32 v156, v44, v45 op_sel:[0,0,1]
	v_cvt_pk_fp8_f32 v157, v48, v49 op_sel:[0,0,1]
	global_load_dword v66, v178, s[100:101] nt
	s_add_u32 s100, s100, s89
	s_addc_u32 s101, s101, 0
	global_load_dword v67, v178, s[100:101] nt
	s_add_u32 s100, s100, s89
	s_addc_u32 s101, s101, 0
	global_load_dword v68, v178, s[100:101] nt
	s_add_u32 s100, s100, s89
	s_addc_u32 s101, s101, 0
	global_load_dword v69, v178, s[100:101] nt
	s_add_u32 s100, s100, s89
	s_addc_u32 s101, s101, 0
	global_load_dword v70, v178, s[100:101] nt
	s_add_u32 s100, s100, s89
	s_addc_u32 s101, s101, 0
	global_load_dword v71, v178, s[100:101] nt
	s_add_u32 s100, s100, s89
	s_addc_u32 s101, s101, 0
	global_load_dword v72, v178, s[100:101] nt
	s_add_u32 s100, s100, s89
	s_addc_u32 s101, s101, 0
	global_load_dword v73, v178, s[100:101] nt
	s_add_u32 s100, s100, s89
	s_addc_u32 s101, s101, 0
	global_load_dword v74, v178, s[100:101] nt
	s_add_u32 s100, s100, s89
	s_addc_u32 s101, s101, 0
	global_load_dword v75, v178, s[100:101] nt
	s_add_u32 s100, s100, s89
	s_addc_u32 s101, s101, 0
	global_load_dword v76, v178, s[100:101] nt
	s_add_u32 s100, s100, s89
	s_addc_u32 s101, s101, 0
	global_load_dword v77, v178, s[100:101] nt
	s_add_u32 s100, s100, s89
	s_addc_u32 s101, s101, 0
	global_load_dword v78, v178, s[100:101] nt
	s_add_u32 s100, s100, s89
	s_addc_u32 s101, s101, 0
	global_load_dword v79, v178, s[100:101] nt
	s_add_u32 s100, s100, s89
	s_addc_u32 s101, s101, 0
	global_load_dword v80, v178, s[100:101] nt
	s_add_u32 s100, s100, s89
	s_addc_u32 s101, s101, 0
	global_load_dword v81, v178, s[100:101] nt
	s_add_u32 s100, s100, s89
	s_addc_u32 s101, s101, 0
	s_waitcnt vmcnt(16)
	v_mul_f32_e32 v50, 0x42000000, v50
	v_mul_f32_e32 v51, 0x42000000, v51
	v_mul_f32_e32 v52, 0x42000000, v52
	v_mul_f32_e32 v53, 0x42000000, v53
	v_mul_f32_e32 v54, 0x42000000, v54
	v_mul_f32_e32 v55, 0x42000000, v55
	v_mul_f32_e32 v56, 0x42000000, v56
	v_mul_f32_e32 v57, 0x42000000, v57
	v_mul_f32_e32 v58, 0x42000000, v58
	v_mul_f32_e32 v59, 0x42000000, v59
	v_mul_f32_e32 v60, 0x42000000, v60
	v_mul_f32_e32 v61, 0x42000000, v61
	v_mul_f32_e32 v62, 0x42000000, v62
	v_mul_f32_e32 v63, 0x42000000, v63
	v_mul_f32_e32 v64, 0x42000000, v64
	v_mul_f32_e32 v65, 0x42000000, v65
	v_cvt_pk_fp8_f32 v158, v50, v51
	v_cvt_pk_fp8_f32 v159, v54, v55
	v_cvt_pk_fp8_f32 v160, v58, v59
	v_cvt_pk_fp8_f32 v161, v62, v63
	v_cvt_pk_fp8_f32 v158, v52, v53 op_sel:[0,0,1]
	v_cvt_pk_fp8_f32 v159, v56, v57 op_sel:[0,0,1]
	v_cvt_pk_fp8_f32 v160, v60, v61 op_sel:[0,0,1]
	v_cvt_pk_fp8_f32 v161, v64, v65 op_sel:[0,0,1]
	global_load_dword v82, v178, s[100:101] nt
	s_add_u32 s100, s100, s89
	s_addc_u32 s101, s101, 0
	global_load_dword v83, v178, s[100:101] nt
	s_add_u32 s100, s100, s89
	s_addc_u32 s101, s101, 0
	global_load_dword v84, v178, s[100:101] nt
	s_add_u32 s100, s100, s89
	s_addc_u32 s101, s101, 0
	global_load_dword v85, v178, s[100:101] nt
	s_add_u32 s100, s100, s89
	s_addc_u32 s101, s101, 0
	global_load_dword v86, v178, s[100:101] nt
	s_add_u32 s100, s100, s89
	s_addc_u32 s101, s101, 0
	global_load_dword v87, v178, s[100:101] nt
	s_add_u32 s100, s100, s89
	s_addc_u32 s101, s101, 0
	global_load_dword v88, v178, s[100:101] nt
	s_add_u32 s100, s100, s89
	s_addc_u32 s101, s101, 0
	global_load_dword v89, v178, s[100:101] nt
	s_add_u32 s100, s100, s89
	s_addc_u32 s101, s101, 0
	global_load_dword v90, v178, s[100:101] nt
	s_add_u32 s100, s100, s89
	s_addc_u32 s101, s101, 0
	global_load_dword v91, v178, s[100:101] nt
	s_add_u32 s100, s100, s89
	s_addc_u32 s101, s101, 0
	global_load_dword v92, v178, s[100:101] nt
	s_add_u32 s100, s100, s89
	s_addc_u32 s101, s101, 0
	global_load_dword v93, v178, s[100:101] nt
	s_add_u32 s100, s100, s89
	s_addc_u32 s101, s101, 0
	global_load_dword v94, v178, s[100:101] nt
	s_add_u32 s100, s100, s89
	s_addc_u32 s101, s101, 0
	global_load_dword v95, v178, s[100:101] nt
	s_add_u32 s100, s100, s89
	s_addc_u32 s101, s101, 0
	global_load_dword v96, v178, s[100:101] nt
	s_add_u32 s100, s100, s89
	s_addc_u32 s101, s101, 0
	global_load_dword v97, v178, s[100:101] nt
	s_add_u32 s100, s100, s89
	s_addc_u32 s101, s101, 0
	s_waitcnt vmcnt(16)
	v_mul_f32_e32 v66, 0x42000000, v66
	v_mul_f32_e32 v67, 0x42000000, v67
	v_mul_f32_e32 v68, 0x42000000, v68
	v_mul_f32_e32 v69, 0x42000000, v69
	v_mul_f32_e32 v70, 0x42000000, v70
	v_mul_f32_e32 v71, 0x42000000, v71
	v_mul_f32_e32 v72, 0x42000000, v72
	v_mul_f32_e32 v73, 0x42000000, v73
	v_mul_f32_e32 v74, 0x42000000, v74
	v_mul_f32_e32 v75, 0x42000000, v75
	v_mul_f32_e32 v76, 0x42000000, v76
	v_mul_f32_e32 v77, 0x42000000, v77
	v_mul_f32_e32 v78, 0x42000000, v78
	v_mul_f32_e32 v79, 0x42000000, v79
	v_mul_f32_e32 v80, 0x42000000, v80
	v_mul_f32_e32 v81, 0x42000000, v81
	v_cvt_pk_fp8_f32 v162, v66, v67
	v_cvt_pk_fp8_f32 v163, v70, v71
	v_cvt_pk_fp8_f32 v164, v74, v75
	v_cvt_pk_fp8_f32 v165, v78, v79
	v_cvt_pk_fp8_f32 v162, v68, v69 op_sel:[0,0,1]
	v_cvt_pk_fp8_f32 v163, v72, v73 op_sel:[0,0,1]
	v_cvt_pk_fp8_f32 v164, v76, v77 op_sel:[0,0,1]
	v_cvt_pk_fp8_f32 v165, v80, v81 op_sel:[0,0,1]
	s_waitcnt vmcnt(0)
	v_mul_f32_e32 v82, 0x42000000, v82
	v_mul_f32_e32 v83, 0x42000000, v83
	v_mul_f32_e32 v84, 0x42000000, v84
	v_mul_f32_e32 v85, 0x42000000, v85
	v_mul_f32_e32 v86, 0x42000000, v86
	v_mul_f32_e32 v87, 0x42000000, v87
	v_mul_f32_e32 v88, 0x42000000, v88
	v_mul_f32_e32 v89, 0x42000000, v89
	v_mul_f32_e32 v90, 0x42000000, v90
	v_mul_f32_e32 v91, 0x42000000, v91
	v_mul_f32_e32 v92, 0x42000000, v92
	v_mul_f32_e32 v93, 0x42000000, v93
	v_mul_f32_e32 v94, 0x42000000, v94
	v_mul_f32_e32 v95, 0x42000000, v95
	v_mul_f32_e32 v96, 0x42000000, v96
	v_mul_f32_e32 v97, 0x42000000, v97
	v_cvt_pk_fp8_f32 v166, v82, v83
	v_cvt_pk_fp8_f32 v167, v86, v87
	v_cvt_pk_fp8_f32 v168, v90, v91
	v_cvt_pk_fp8_f32 v169, v94, v95
	v_cvt_pk_fp8_f32 v166, v84, v85 op_sel:[0,0,1]
	v_cvt_pk_fp8_f32 v167, v88, v89 op_sel:[0,0,1]
	v_cvt_pk_fp8_f32 v168, v92, v93 op_sel:[0,0,1]
	v_cvt_pk_fp8_f32 v169, v96, v97 op_sel:[0,0,1]
	s_mov_b32 vcc_lo, 0xaaaaaaaa
	s_mov_b32 vcc_hi, 0xaaaaaaaa
	s_nop 1
	v_cndmask_b32_dpp v170, v154, v158, vcc quad_perm:[1,0,3,2] row_mask:0xf bank_mask:0xf
	v_cndmask_b32_dpp v174, v162, v166, vcc quad_perm:[1,0,3,2] row_mask:0xf bank_mask:0xf
	v_cndmask_b32_dpp v171, v155, v159, vcc quad_perm:[1,0,3,2] row_mask:0xf bank_mask:0xf
	v_cndmask_b32_dpp v175, v163, v167, vcc quad_perm:[1,0,3,2] row_mask:0xf bank_mask:0xf
	v_cndmask_b32_dpp v172, v156, v160, vcc quad_perm:[1,0,3,2] row_mask:0xf bank_mask:0xf
	v_cndmask_b32_dpp v176, v164, v168, vcc quad_perm:[1,0,3,2] row_mask:0xf bank_mask:0xf
	v_cndmask_b32_dpp v173, v157, v161, vcc quad_perm:[1,0,3,2] row_mask:0xf bank_mask:0xf
	v_cndmask_b32_dpp v177, v165, v169, vcc quad_perm:[1,0,3,2] row_mask:0xf bank_mask:0xf
	s_mov_b32 vcc_lo, 0x55555555
	s_mov_b32 vcc_hi, 0x55555555
	s_nop 1
	v_cndmask_b32_dpp v154, v158, v154, vcc quad_perm:[1,0,3,2] row_mask:0xf bank_mask:0xf
	v_cndmask_b32_dpp v162, v166, v162, vcc quad_perm:[1,0,3,2] row_mask:0xf bank_mask:0xf
	v_cndmask_b32_dpp v155, v159, v155, vcc quad_perm:[1,0,3,2] row_mask:0xf bank_mask:0xf
	v_cndmask_b32_dpp v163, v167, v163, vcc quad_perm:[1,0,3,2] row_mask:0xf bank_mask:0xf
	v_cndmask_b32_dpp v156, v160, v156, vcc quad_perm:[1,0,3,2] row_mask:0xf bank_mask:0xf
	v_cndmask_b32_dpp v164, v168, v164, vcc quad_perm:[1,0,3,2] row_mask:0xf bank_mask:0xf
	v_cndmask_b32_dpp v157, v161, v157, vcc quad_perm:[1,0,3,2] row_mask:0xf bank_mask:0xf
	v_cndmask_b32_dpp v165, v169, v165, vcc quad_perm:[1,0,3,2] row_mask:0xf bank_mask:0xf
	s_mov_b32 vcc_lo, 0xcccccccc
	s_mov_b32 vcc_hi, 0xcccccccc
	s_nop 1
	v_cndmask_b32_dpp v158, v154, v162, vcc quad_perm:[2,3,0,1] row_mask:0xf bank_mask:0xf
	v_cndmask_b32_dpp v166, v170, v174, vcc quad_perm:[2,3,0,1] row_mask:0xf bank_mask:0xf
	v_cndmask_b32_dpp v159, v155, v163, vcc quad_perm:[2,3,0,1] row_mask:0xf bank_mask:0xf
	v_cndmask_b32_dpp v167, v171, v175, vcc quad_perm:[2,3,0,1] row_mask:0xf bank_mask:0xf
	v_cndmask_b32_dpp v160, v156, v164, vcc quad_perm:[2,3,0,1] row_mask:0xf bank_mask:0xf
	v_cndmask_b32_dpp v168, v172, v176, vcc quad_perm:[2,3,0,1] row_mask:0xf bank_mask:0xf
	v_cndmask_b32_dpp v161, v157, v165, vcc quad_perm:[2,3,0,1] row_mask:0xf bank_mask:0xf
	v_cndmask_b32_dpp v169, v173, v177, vcc quad_perm:[2,3,0,1] row_mask:0xf bank_mask:0xf
	s_mov_b32 vcc_lo, 0x33333333
	s_mov_b32 vcc_hi, 0x33333333
	s_nop 1
	v_cndmask_b32_dpp v154, v162, v154, vcc quad_perm:[2,3,0,1] row_mask:0xf bank_mask:0xf
	v_cndmask_b32_dpp v170, v174, v170, vcc quad_perm:[2,3,0,1] row_mask:0xf bank_mask:0xf
	v_cndmask_b32_dpp v155, v163, v155, vcc quad_perm:[2,3,0,1] row_mask:0xf bank_mask:0xf
	v_cndmask_b32_dpp v171, v175, v171, vcc quad_perm:[2,3,0,1] row_mask:0xf bank_mask:0xf
	v_cndmask_b32_dpp v156, v164, v156, vcc quad_perm:[2,3,0,1] row_mask:0xf bank_mask:0xf
	v_cndmask_b32_dpp v172, v176, v172, vcc quad_perm:[2,3,0,1] row_mask:0xf bank_mask:0xf
	v_cndmask_b32_dpp v157, v165, v157, vcc quad_perm:[2,3,0,1] row_mask:0xf bank_mask:0xf
	v_cndmask_b32_dpp v173, v177, v173, vcc quad_perm:[2,3,0,1] row_mask:0xf bank_mask:0xf
	global_store_dwordx4 v179, v[154:157], s[82:83] nt
	global_store_dwordx4 v180, v[170:173], s[82:83] nt
	global_store_dwordx4 v181, v[158:161], s[82:83] nt
	global_store_dwordx4 v190, v[166:169], s[82:83] nt

.Lhw_go_s1_0:
	s_add_u32 s100, s82, s69
	s_addc_u32 s101, s83, 0
	v_readlane_b32 s82, v239, 44
	v_readlane_b32 s83, v239, 45
	s_add_u32 s82, s82, s98
	s_addc_u32 s83, s83, 0
	global_load_dword v34, v178, s[100:101] nt
	s_add_u32 s100, s100, s89
	s_addc_u32 s101, s101, 0
	global_load_dword v35, v178, s[100:101] nt
	s_add_u32 s100, s100, s89
	s_addc_u32 s101, s101, 0
	global_load_dword v36, v178, s[100:101] nt
	s_add_u32 s100, s100, s89
	s_addc_u32 s101, s101, 0
	global_load_dword v37, v178, s[100:101] nt
	s_add_u32 s100, s100, s89
	s_addc_u32 s101, s101, 0
	global_load_dword v38, v178, s[100:101] nt
	s_add_u32 s100, s100, s89
	s_addc_u32 s101, s101, 0
	global_load_dword v39, v178, s[100:101] nt
	s_add_u32 s100, s100, s89
	s_addc_u32 s101, s101, 0
	global_load_dword v40, v178, s[100:101] nt
	s_add_u32 s100, s100, s89
	s_addc_u32 s101, s101, 0
	global_load_dword v41, v178, s[100:101] nt
	s_add_u32 s100, s100, s89
	s_addc_u32 s101, s101, 0
	global_load_dword v42, v178, s[100:101] nt
	s_add_u32 s100, s100, s89
	s_addc_u32 s101, s101, 0
	global_load_dword v43, v178, s[100:101] nt
	s_add_u32 s100, s100, s89
	s_addc_u32 s101, s101, 0
	global_load_dword v44, v178, s[100:101] nt
	s_add_u32 s100, s100, s89
	s_addc_u32 s101, s101, 0
	global_load_dword v45, v178, s[100:101] nt
	s_add_u32 s100, s100, s89
	s_addc_u32 s101, s101, 0
	global_load_dword v46, v178, s[100:101] nt
	s_add_u32 s100, s100, s89
	s_addc_u32 s101, s101, 0
	global_load_dword v47, v178, s[100:101] nt
	s_add_u32 s100, s100, s89
	s_addc_u32 s101, s101, 0
	global_load_dword v48, v178, s[100:101] nt
	s_add_u32 s100, s100, s89
	s_addc_u32 s101, s101, 0
	global_load_dword v49, v178, s[100:101] nt
	s_add_u32 s100, s100, s89
	s_addc_u32 s101, s101, 0
	global_load_dword v50, v178, s[100:101] nt
	s_add_u32 s100, s100, s89
	s_addc_u32 s101, s101, 0
	global_load_dword v51, v178, s[100:101] nt
	s_add_u32 s100, s100, s89
	s_addc_u32 s101, s101, 0
	global_load_dword v52, v178, s[100:101] nt
	s_add_u32 s100, s100, s89
	s_addc_u32 s101, s101, 0
	global_load_dword v53, v178, s[100:101] nt
	s_add_u32 s100, s100, s89
	s_addc_u32 s101, s101, 0
	global_load_dword v54, v178, s[100:101] nt
	s_add_u32 s100, s100, s89
	s_addc_u32 s101, s101, 0
	global_load_dword v55, v178, s[100:101] nt
	s_add_u32 s100, s100, s89
	s_addc_u32 s101, s101, 0
	global_load_dword v56, v178, s[100:101] nt
	s_add_u32 s100, s100, s89
	s_addc_u32 s101, s101, 0
	global_load_dword v57, v178, s[100:101] nt
	s_add_u32 s100, s100, s89
	s_addc_u32 s101, s101, 0
	global_load_dword v58, v178, s[100:101] nt
	s_add_u32 s100, s100, s89
	s_addc_u32 s101, s101, 0
	global_load_dword v59, v178, s[100:101] nt
	s_add_u32 s100, s100, s89
	s_addc_u32 s101, s101, 0
	global_load_dword v60, v178, s[100:101] nt
	s_add_u32 s100, s100, s89
	s_addc_u32 s101, s101, 0
	global_load_dword v61, v178, s[100:101] nt
	s_add_u32 s100, s100, s89
	s_addc_u32 s101, s101, 0
	global_load_dword v62, v178, s[100:101] nt
	s_add_u32 s100, s100, s89
	s_addc_u32 s101, s101, 0
	global_load_dword v63, v178, s[100:101] nt
	s_add_u32 s100, s100, s89
	s_addc_u32 s101, s101, 0
	global_load_dword v64, v178, s[100:101] nt
	s_add_u32 s100, s100, s89
	s_addc_u32 s101, s101, 0
	global_load_dword v65, v178, s[100:101] nt
	s_add_u32 s100, s100, s89
	s_addc_u32 s101, s101, 0
	s_waitcnt vmcnt(16)
	v_mul_f32_e32 v34, 0x42000000, v34
	v_mul_f32_e32 v35, 0x42000000, v35
	v_mul_f32_e32 v36, 0x42000000, v36
	v_mul_f32_e32 v37, 0x42000000, v37
	v_mul_f32_e32 v38, 0x42000000, v38
	v_mul_f32_e32 v39, 0x42000000, v39
	v_mul_f32_e32 v40, 0x42000000, v40
	v_mul_f32_e32 v41, 0x42000000, v41
	v_mul_f32_e32 v42, 0x42000000, v42
	v_mul_f32_e32 v43, 0x42000000, v43
	v_mul_f32_e32 v44, 0x42000000, v44
	v_mul_f32_e32 v45, 0x42000000, v45
	v_mul_f32_e32 v46, 0x42000000, v46
	v_mul_f32_e32 v47, 0x42000000, v47
	v_mul_f32_e32 v48, 0x42000000, v48
	v_mul_f32_e32 v49, 0x42000000, v49
	v_cvt_pk_fp8_f32 v154, v34, v35
	v_cvt_pk_fp8_f32 v155, v38, v39
	v_cvt_pk_fp8_f32 v156, v42, v43
	v_cvt_pk_fp8_f32 v157, v46, v47
	v_cvt_pk_fp8_f32 v154, v36, v37 op_sel:[0,0,1]
	v_cvt_pk_fp8_f32 v155, v40, v41 op_sel:[0,0,1]
	v_cvt_pk_fp8_f32 v156, v44, v45 op_sel:[0,0,1]
	v_cvt_pk_fp8_f32 v157, v48, v49 op_sel:[0,0,1]
	global_load_dword v66, v178, s[100:101] nt
	s_add_u32 s100, s100, s89
	s_addc_u32 s101, s101, 0
	global_load_dword v67, v178, s[100:101] nt
	s_add_u32 s100, s100, s89
	s_addc_u32 s101, s101, 0
	global_load_dword v68, v178, s[100:101] nt
	s_add_u32 s100, s100, s89
	s_addc_u32 s101, s101, 0
	global_load_dword v69, v178, s[100:101] nt
	s_add_u32 s100, s100, s89
	s_addc_u32 s101, s101, 0
	global_load_dword v70, v178, s[100:101] nt
	s_add_u32 s100, s100, s89
	s_addc_u32 s101, s101, 0
	global_load_dword v71, v178, s[100:101] nt
	s_add_u32 s100, s100, s89
	s_addc_u32 s101, s101, 0
	global_load_dword v72, v178, s[100:101] nt
	s_add_u32 s100, s100, s89
	s_addc_u32 s101, s101, 0
	global_load_dword v73, v178, s[100:101] nt
	s_add_u32 s100, s100, s89
	s_addc_u32 s101, s101, 0
	global_load_dword v74, v178, s[100:101] nt
	s_add_u32 s100, s100, s89
	s_addc_u32 s101, s101, 0
	global_load_dword v75, v178, s[100:101] nt
	s_add_u32 s100, s100, s89
	s_addc_u32 s101, s101, 0
	global_load_dword v76, v178, s[100:101] nt
	s_add_u32 s100, s100, s89
	s_addc_u32 s101, s101, 0
	global_load_dword v77, v178, s[100:101] nt
	s_add_u32 s100, s100, s89
	s_addc_u32 s101, s101, 0
	global_load_dword v78, v178, s[100:101] nt
	s_add_u32 s100, s100, s89
	s_addc_u32 s101, s101, 0
	global_load_dword v79, v178, s[100:101] nt
	s_add_u32 s100, s100, s89
	s_addc_u32 s101, s101, 0
	global_load_dword v80, v178, s[100:101] nt
	s_add_u32 s100, s100, s89
	s_addc_u32 s101, s101, 0
	global_load_dword v81, v178, s[100:101] nt
	s_add_u32 s100, s100, s89
	s_addc_u32 s101, s101, 0
	s_waitcnt vmcnt(16)
	v_mul_f32_e32 v50, 0x42000000, v50
	v_mul_f32_e32 v51, 0x42000000, v51
	v_mul_f32_e32 v52, 0x42000000, v52
	v_mul_f32_e32 v53, 0x42000000, v53
	v_mul_f32_e32 v54, 0x42000000, v54
	v_mul_f32_e32 v55, 0x42000000, v55
	v_mul_f32_e32 v56, 0x42000000, v56
	v_mul_f32_e32 v57, 0x42000000, v57
	v_mul_f32_e32 v58, 0x42000000, v58
	v_mul_f32_e32 v59, 0x42000000, v59
	v_mul_f32_e32 v60, 0x42000000, v60
	v_mul_f32_e32 v61, 0x42000000, v61
	v_mul_f32_e32 v62, 0x42000000, v62
	v_mul_f32_e32 v63, 0x42000000, v63
	v_mul_f32_e32 v64, 0x42000000, v64
	v_mul_f32_e32 v65, 0x42000000, v65
	v_cvt_pk_fp8_f32 v158, v50, v51
	v_cvt_pk_fp8_f32 v159, v54, v55
	v_cvt_pk_fp8_f32 v160, v58, v59
	v_cvt_pk_fp8_f32 v161, v62, v63
	v_cvt_pk_fp8_f32 v158, v52, v53 op_sel:[0,0,1]
	v_cvt_pk_fp8_f32 v159, v56, v57 op_sel:[0,0,1]
	v_cvt_pk_fp8_f32 v160, v60, v61 op_sel:[0,0,1]
	v_cvt_pk_fp8_f32 v161, v64, v65 op_sel:[0,0,1]
	global_load_dword v82, v178, s[100:101] nt
	s_add_u32 s100, s100, s89
	s_addc_u32 s101, s101, 0
	global_load_dword v83, v178, s[100:101] nt
	s_add_u32 s100, s100, s89
	s_addc_u32 s101, s101, 0
	global_load_dword v84, v178, s[100:101] nt
	s_add_u32 s100, s100, s89
	s_addc_u32 s101, s101, 0
	global_load_dword v85, v178, s[100:101] nt
	s_add_u32 s100, s100, s89
	s_addc_u32 s101, s101, 0
	global_load_dword v86, v178, s[100:101] nt
	s_add_u32 s100, s100, s89
	s_addc_u32 s101, s101, 0
	global_load_dword v87, v178, s[100:101] nt
	s_add_u32 s100, s100, s89
	s_addc_u32 s101, s101, 0
	global_load_dword v88, v178, s[100:101] nt
	s_add_u32 s100, s100, s89
	s_addc_u32 s101, s101, 0
	global_load_dword v89, v178, s[100:101] nt
	s_add_u32 s100, s100, s89
	s_addc_u32 s101, s101, 0
	global_load_dword v90, v178, s[100:101] nt
	s_add_u32 s100, s100, s89
	s_addc_u32 s101, s101, 0
	global_load_dword v91, v178, s[100:101] nt
	s_add_u32 s100, s100, s89
	s_addc_u32 s101, s101, 0
	global_load_dword v92, v178, s[100:101] nt
	s_add_u32 s100, s100, s89
	s_addc_u32 s101, s101, 0
	global_load_dword v93, v178, s[100:101] nt
	s_add_u32 s100, s100, s89
	s_addc_u32 s101, s101, 0
	global_load_dword v94, v178, s[100:101] nt
	s_add_u32 s100, s100, s89
	s_addc_u32 s101, s101, 0
	global_load_dword v95, v178, s[100:101] nt
	s_add_u32 s100, s100, s89
	s_addc_u32 s101, s101, 0
	global_load_dword v96, v178, s[100:101] nt
	s_add_u32 s100, s100, s89
	s_addc_u32 s101, s101, 0
	global_load_dword v97, v178, s[100:101] nt
	s_add_u32 s100, s100, s89
	s_addc_u32 s101, s101, 0
	s_waitcnt vmcnt(16)
	v_mul_f32_e32 v66, 0x42000000, v66
	v_mul_f32_e32 v67, 0x42000000, v67
	v_mul_f32_e32 v68, 0x42000000, v68
	v_mul_f32_e32 v69, 0x42000000, v69
	v_mul_f32_e32 v70, 0x42000000, v70
	v_mul_f32_e32 v71, 0x42000000, v71
	v_mul_f32_e32 v72, 0x42000000, v72
	v_mul_f32_e32 v73, 0x42000000, v73
	v_mul_f32_e32 v74, 0x42000000, v74
	v_mul_f32_e32 v75, 0x42000000, v75
	v_mul_f32_e32 v76, 0x42000000, v76
	v_mul_f32_e32 v77, 0x42000000, v77
	v_mul_f32_e32 v78, 0x42000000, v78
	v_mul_f32_e32 v79, 0x42000000, v79
	v_mul_f32_e32 v80, 0x42000000, v80
	v_mul_f32_e32 v81, 0x42000000, v81
	v_cvt_pk_fp8_f32 v162, v66, v67
	v_cvt_pk_fp8_f32 v163, v70, v71
	v_cvt_pk_fp8_f32 v164, v74, v75
	v_cvt_pk_fp8_f32 v165, v78, v79
	v_cvt_pk_fp8_f32 v162, v68, v69 op_sel:[0,0,1]
	v_cvt_pk_fp8_f32 v163, v72, v73 op_sel:[0,0,1]
	v_cvt_pk_fp8_f32 v164, v76, v77 op_sel:[0,0,1]
	v_cvt_pk_fp8_f32 v165, v80, v81 op_sel:[0,0,1]
	s_waitcnt vmcnt(0)
	v_mul_f32_e32 v82, 0x42000000, v82
	v_mul_f32_e32 v83, 0x42000000, v83
	v_mul_f32_e32 v84, 0x42000000, v84
	v_mul_f32_e32 v85, 0x42000000, v85
	v_mul_f32_e32 v86, 0x42000000, v86
	v_mul_f32_e32 v87, 0x42000000, v87
	v_mul_f32_e32 v88, 0x42000000, v88
	v_mul_f32_e32 v89, 0x42000000, v89
	v_mul_f32_e32 v90, 0x42000000, v90
	v_mul_f32_e32 v91, 0x42000000, v91
	v_mul_f32_e32 v92, 0x42000000, v92
	v_mul_f32_e32 v93, 0x42000000, v93
	v_mul_f32_e32 v94, 0x42000000, v94
	v_mul_f32_e32 v95, 0x42000000, v95
	v_mul_f32_e32 v96, 0x42000000, v96
	v_mul_f32_e32 v97, 0x42000000, v97
	v_cvt_pk_fp8_f32 v166, v82, v83
	v_cvt_pk_fp8_f32 v167, v86, v87
	v_cvt_pk_fp8_f32 v168, v90, v91
	v_cvt_pk_fp8_f32 v169, v94, v95
	v_cvt_pk_fp8_f32 v166, v84, v85 op_sel:[0,0,1]
	v_cvt_pk_fp8_f32 v167, v88, v89 op_sel:[0,0,1]
	v_cvt_pk_fp8_f32 v168, v92, v93 op_sel:[0,0,1]
	v_cvt_pk_fp8_f32 v169, v96, v97 op_sel:[0,0,1]
	s_mov_b32 vcc_lo, 0xaaaaaaaa
	s_mov_b32 vcc_hi, 0xaaaaaaaa
	s_nop 1
	v_cndmask_b32_dpp v170, v154, v158, vcc quad_perm:[1,0,3,2] row_mask:0xf bank_mask:0xf
	v_cndmask_b32_dpp v174, v162, v166, vcc quad_perm:[1,0,3,2] row_mask:0xf bank_mask:0xf
	v_cndmask_b32_dpp v171, v155, v159, vcc quad_perm:[1,0,3,2] row_mask:0xf bank_mask:0xf
	v_cndmask_b32_dpp v175, v163, v167, vcc quad_perm:[1,0,3,2] row_mask:0xf bank_mask:0xf
	v_cndmask_b32_dpp v172, v156, v160, vcc quad_perm:[1,0,3,2] row_mask:0xf bank_mask:0xf
	v_cndmask_b32_dpp v176, v164, v168, vcc quad_perm:[1,0,3,2] row_mask:0xf bank_mask:0xf
	v_cndmask_b32_dpp v173, v157, v161, vcc quad_perm:[1,0,3,2] row_mask:0xf bank_mask:0xf
	v_cndmask_b32_dpp v177, v165, v169, vcc quad_perm:[1,0,3,2] row_mask:0xf bank_mask:0xf
	s_mov_b32 vcc_lo, 0x55555555
	s_mov_b32 vcc_hi, 0x55555555
	s_nop 1
	v_cndmask_b32_dpp v154, v158, v154, vcc quad_perm:[1,0,3,2] row_mask:0xf bank_mask:0xf
	v_cndmask_b32_dpp v162, v166, v162, vcc quad_perm:[1,0,3,2] row_mask:0xf bank_mask:0xf
	v_cndmask_b32_dpp v155, v159, v155, vcc quad_perm:[1,0,3,2] row_mask:0xf bank_mask:0xf
	v_cndmask_b32_dpp v163, v167, v163, vcc quad_perm:[1,0,3,2] row_mask:0xf bank_mask:0xf
	v_cndmask_b32_dpp v156, v160, v156, vcc quad_perm:[1,0,3,2] row_mask:0xf bank_mask:0xf
	v_cndmask_b32_dpp v164, v168, v164, vcc quad_perm:[1,0,3,2] row_mask:0xf bank_mask:0xf
	v_cndmask_b32_dpp v157, v161, v157, vcc quad_perm:[1,0,3,2] row_mask:0xf bank_mask:0xf
	v_cndmask_b32_dpp v165, v169, v165, vcc quad_perm:[1,0,3,2] row_mask:0xf bank_mask:0xf
	s_mov_b32 vcc_lo, 0xcccccccc
	s_mov_b32 vcc_hi, 0xcccccccc
	s_nop 1
	v_cndmask_b32_dpp v158, v154, v162, vcc quad_perm:[2,3,0,1] row_mask:0xf bank_mask:0xf
	v_cndmask_b32_dpp v166, v170, v174, vcc quad_perm:[2,3,0,1] row_mask:0xf bank_mask:0xf
	v_cndmask_b32_dpp v159, v155, v163, vcc quad_perm:[2,3,0,1] row_mask:0xf bank_mask:0xf
	v_cndmask_b32_dpp v167, v171, v175, vcc quad_perm:[2,3,0,1] row_mask:0xf bank_mask:0xf
	v_cndmask_b32_dpp v160, v156, v164, vcc quad_perm:[2,3,0,1] row_mask:0xf bank_mask:0xf
	v_cndmask_b32_dpp v168, v172, v176, vcc quad_perm:[2,3,0,1] row_mask:0xf bank_mask:0xf
	v_cndmask_b32_dpp v161, v157, v165, vcc quad_perm:[2,3,0,1] row_mask:0xf bank_mask:0xf
	v_cndmask_b32_dpp v169, v173, v177, vcc quad_perm:[2,3,0,1] row_mask:0xf bank_mask:0xf
	s_mov_b32 vcc_lo, 0x33333333
	s_mov_b32 vcc_hi, 0x33333333
	s_nop 1
	v_cndmask_b32_dpp v154, v162, v154, vcc quad_perm:[2,3,0,1] row_mask:0xf bank_mask:0xf
	v_cndmask_b32_dpp v170, v174, v170, vcc quad_perm:[2,3,0,1] row_mask:0xf bank_mask:0xf
	v_cndmask_b32_dpp v155, v163, v155, vcc quad_perm:[2,3,0,1] row_mask:0xf bank_mask:0xf
	v_cndmask_b32_dpp v171, v175, v171, vcc quad_perm:[2,3,0,1] row_mask:0xf bank_mask:0xf
	v_cndmask_b32_dpp v156, v164, v156, vcc quad_perm:[2,3,0,1] row_mask:0xf bank_mask:0xf
	v_cndmask_b32_dpp v172, v176, v172, vcc quad_perm:[2,3,0,1] row_mask:0xf bank_mask:0xf
	v_cndmask_b32_dpp v157, v165, v157, vcc quad_perm:[2,3,0,1] row_mask:0xf bank_mask:0xf
	v_cndmask_b32_dpp v173, v177, v173, vcc quad_perm:[2,3,0,1] row_mask:0xf bank_mask:0xf
	global_store_dwordx4 v179, v[154:157], s[82:83] nt
	global_store_dwordx4 v180, v[170:173], s[82:83] nt
	global_store_dwordx4 v181, v[158:161], s[82:83] nt
	global_store_dwordx4 v190, v[166:169], s[82:83] nt
	v_readlane_b32 s2, v239, 0
	s_lshr_b32 s2, s2, 6
	s_add_i32 s2, s2, 6
	s_cmp_gt_u32 s2, 13
	s_cbranch_scc1 .Lhw_seam1_done
	s_add_i32 s2, s2, 14
	s_mul_i32 s2, s2, s74
	v_readlane_b32 s9, v239, 23
	s_lshr_b32 s9, s9, 3
	s_add_i32 s2, s2, s9
	s_cmp_gt_u32 s2, 24575
	s_cbranch_scc1 .Lhw_seam1_done
	v_mbcnt_lo_u32_b32 v178, -1, 0
	v_mbcnt_hi_u32_b32 v178, -1, v178
	v_and_b32_e32 v179, 60, v178
	v_lshlrev_b32_e32 v179, 10, v179
	v_and_b32_e32 v180, 3, v178
	v_lshl_or_b32 v179, v180, 4, v179
	v_add_u32_e32 v180, 0x400, v179
	v_add_u32_e32 v181, 0x800, v179
	v_add_u32_e32 v190, 0xc00, v179
	v_lshlrev_b32_e32 v178, 2, v178
	s_cmp_lt_u32 s2, 16384
	s_cbranch_scc0 .Lhw_dn_s1_1
	s_lshr_b32 s9, s2, 9
	s_bfe_u32 s32, s2, 0x40005
	s_and_b32 s53, s2, 31
	s_lshl_b32 s69, s9, 23
	s_lshl_b32 s100, s32, 19
	s_add_i32 s69, s69, s100
	s_lshl_b32 s100, s53, 8
	s_add_i32 s69, s69, s100
	s_lshl_b32 s98, s9, 11
	s_bfe_u32 s100, s53, 0x30001
	s_lshl_b32 s100, s100, 8
	s_add_i32 s98, s98, s100
	s_lshr_b32 s100, s53, 4
	s_lshl_b32 s100, s100, 7
	s_add_i32 s98, s98, s100
	s_and_b32 s100, s53, 1
	s_lshl_b32 s100, s100, 6
	s_add_i32 s98, s98, s100
	s_lshl_b32 s98, s98, 10
	s_lshl_b32 s100, s32, 6
	s_add_i32 s98, s98, s100
	s_add_i32 s98, s98, 0x2000000
	v_readlane_b32 s82, v239, 11
	v_readlane_b32 s83, v239, 12
	s_movk_i32 s89, 8192
	s_branch .Lhw_go_s1_1

.Lhw_go_s2_0:
	s_add_u32 s100, s82, s69
	s_addc_u32 s101, s83, 0
	v_readlane_b32 s82, v239, 44
	v_readlane_b32 s83, v239, 45
	s_add_u32 s82, s82, s98
	s_addc_u32 s83, s83, 0
	global_load_dword v34, v178, s[100:101] nt
	s_add_u32 s100, s100, s89
	s_addc_u32 s101, s101, 0
	global_load_dword v35, v178, s[100:101] nt
	s_add_u32 s100, s100, s89
	s_addc_u32 s101, s101, 0
	global_load_dword v36, v178, s[100:101] nt
	s_add_u32 s100, s100, s89
	s_addc_u32 s101, s101, 0
	global_load_dword v37, v178, s[100:101] nt
	s_add_u32 s100, s100, s89
	s_addc_u32 s101, s101, 0
	global_load_dword v38, v178, s[100:101] nt
	s_add_u32 s100, s100, s89
	s_addc_u32 s101, s101, 0
	global_load_dword v39, v178, s[100:101] nt
	s_add_u32 s100, s100, s89
	s_addc_u32 s101, s101, 0
	global_load_dword v40, v178, s[100:101] nt
	s_add_u32 s100, s100, s89
	s_addc_u32 s101, s101, 0
	global_load_dword v41, v178, s[100:101] nt
	s_add_u32 s100, s100, s89
	s_addc_u32 s101, s101, 0
	global_load_dword v42, v178, s[100:101] nt
	s_add_u32 s100, s100, s89
	s_addc_u32 s101, s101, 0
	global_load_dword v43, v178, s[100:101] nt
	s_add_u32 s100, s100, s89
	s_addc_u32 s101, s101, 0
	global_load_dword v44, v178, s[100:101] nt
	s_add_u32 s100, s100, s89
	s_addc_u32 s101, s101, 0
	global_load_dword v45, v178, s[100:101] nt
	s_add_u32 s100, s100, s89
	s_addc_u32 s101, s101, 0
	global_load_dword v46, v178, s[100:101] nt
	s_add_u32 s100, s100, s89
	s_addc_u32 s101, s101, 0
	global_load_dword v47, v178, s[100:101] nt
	s_add_u32 s100, s100, s89
	s_addc_u32 s101, s101, 0
	global_load_dword v48, v178, s[100:101] nt
	s_add_u32 s100, s100, s89
	s_addc_u32 s101, s101, 0
	global_load_dword v49, v178, s[100:101] nt
	s_add_u32 s100, s100, s89
	s_addc_u32 s101, s101, 0
	global_load_dword v50, v178, s[100:101] nt
	s_add_u32 s100, s100, s89
	s_addc_u32 s101, s101, 0
	global_load_dword v51, v178, s[100:101] nt
	s_add_u32 s100, s100, s89
	s_addc_u32 s101, s101, 0
	global_load_dword v52, v178, s[100:101] nt
	s_add_u32 s100, s100, s89
	s_addc_u32 s101, s101, 0
	global_load_dword v53, v178, s[100:101] nt
	s_add_u32 s100, s100, s89
	s_addc_u32 s101, s101, 0
	global_load_dword v54, v178, s[100:101] nt
	s_add_u32 s100, s100, s89
	s_addc_u32 s101, s101, 0
	global_load_dword v55, v178, s[100:101] nt
	s_add_u32 s100, s100, s89
	s_addc_u32 s101, s101, 0
	global_load_dword v56, v178, s[100:101] nt
	s_add_u32 s100, s100, s89
	s_addc_u32 s101, s101, 0
	global_load_dword v57, v178, s[100:101] nt
	s_add_u32 s100, s100, s89
	s_addc_u32 s101, s101, 0
	global_load_dword v58, v178, s[100:101] nt
	s_add_u32 s100, s100, s89
	s_addc_u32 s101, s101, 0
	global_load_dword v59, v178, s[100:101] nt
	s_add_u32 s100, s100, s89
	s_addc_u32 s101, s101, 0
	global_load_dword v60, v178, s[100:101] nt
	s_add_u32 s100, s100, s89
	s_addc_u32 s101, s101, 0
	global_load_dword v61, v178, s[100:101] nt
	s_add_u32 s100, s100, s89
	s_addc_u32 s101, s101, 0
	global_load_dword v62, v178, s[100:101] nt
	s_add_u32 s100, s100, s89
	s_addc_u32 s101, s101, 0
	global_load_dword v63, v178, s[100:101] nt
	s_add_u32 s100, s100, s89
	s_addc_u32 s101, s101, 0
	global_load_dword v64, v178, s[100:101] nt
	s_add_u32 s100, s100, s89
	s_addc_u32 s101, s101, 0
	global_load_dword v65, v178, s[100:101] nt
	s_add_u32 s100, s100, s89
	s_addc_u32 s101, s101, 0
	s_waitcnt vmcnt(16)
	v_mul_f32_e32 v34, 0x42000000, v34
	v_mul_f32_e32 v35, 0x42000000, v35
	v_mul_f32_e32 v36, 0x42000000, v36
	v_mul_f32_e32 v37, 0x42000000, v37
	v_mul_f32_e32 v38, 0x42000000, v38
	v_mul_f32_e32 v39, 0x42000000, v39
	v_mul_f32_e32 v40, 0x42000000, v40
	v_mul_f32_e32 v41, 0x42000000, v41
	v_mul_f32_e32 v42, 0x42000000, v42
	v_mul_f32_e32 v43, 0x42000000, v43
	v_mul_f32_e32 v44, 0x42000000, v44
	v_mul_f32_e32 v45, 0x42000000, v45
	v_mul_f32_e32 v46, 0x42000000, v46
	v_mul_f32_e32 v47, 0x42000000, v47
	v_mul_f32_e32 v48, 0x42000000, v48
	v_mul_f32_e32 v49, 0x42000000, v49
	v_cvt_pk_fp8_f32 v154, v34, v35
	v_cvt_pk_fp8_f32 v155, v38, v39
	v_cvt_pk_fp8_f32 v156, v42, v43
	v_cvt_pk_fp8_f32 v157, v46, v47
	v_cvt_pk_fp8_f32 v154, v36, v37 op_sel:[0,0,1]
	v_cvt_pk_fp8_f32 v155, v40, v41 op_sel:[0,0,1]
	v_cvt_pk_fp8_f32 v156, v44, v45 op_sel:[0,0,1]
	v_cvt_pk_fp8_f32 v157, v48, v49 op_sel:[0,0,1]
	global_load_dword v66, v178, s[100:101] nt
	s_add_u32 s100, s100, s89
	s_addc_u32 s101, s101, 0
	global_load_dword v67, v178, s[100:101] nt
	s_add_u32 s100, s100, s89
	s_addc_u32 s101, s101, 0
	global_load_dword v68, v178, s[100:101] nt
	s_add_u32 s100, s100, s89
	s_addc_u32 s101, s101, 0
	global_load_dword v69, v178, s[100:101] nt
	s_add_u32 s100, s100, s89
	s_addc_u32 s101, s101, 0
	global_load_dword v70, v178, s[100:101] nt
	s_add_u32 s100, s100, s89
	s_addc_u32 s101, s101, 0
	global_load_dword v71, v178, s[100:101] nt
	s_add_u32 s100, s100, s89
	s_addc_u32 s101, s101, 0
	global_load_dword v72, v178, s[100:101] nt
	s_add_u32 s100, s100, s89
	s_addc_u32 s101, s101, 0
	global_load_dword v73, v178, s[100:101] nt
	s_add_u32 s100, s100, s89
	s_addc_u32 s101, s101, 0
	global_load_dword v74, v178, s[100:101] nt
	s_add_u32 s100, s100, s89
	s_addc_u32 s101, s101, 0
	global_load_dword v75, v178, s[100:101] nt
	s_add_u32 s100, s100, s89
	s_addc_u32 s101, s101, 0
	global_load_dword v76, v178, s[100:101] nt
	s_add_u32 s100, s100, s89
	s_addc_u32 s101, s101, 0
	global_load_dword v77, v178, s[100:101] nt
	s_add_u32 s100, s100, s89
	s_addc_u32 s101, s101, 0
	global_load_dword v78, v178, s[100:101] nt
	s_add_u32 s100, s100, s89
	s_addc_u32 s101, s101, 0
	global_load_dword v79, v178, s[100:101] nt
	s_add_u32 s100, s100, s89
	s_addc_u32 s101, s101, 0
	global_load_dword v80, v178, s[100:101] nt
	s_add_u32 s100, s100, s89
	s_addc_u32 s101, s101, 0
	global_load_dword v81, v178, s[100:101] nt
	s_add_u32 s100, s100, s89
	s_addc_u32 s101, s101, 0
	s_waitcnt vmcnt(16)
	v_mul_f32_e32 v50, 0x42000000, v50
	v_mul_f32_e32 v51, 0x42000000, v51
	v_mul_f32_e32 v52, 0x42000000, v52
	v_mul_f32_e32 v53, 0x42000000, v53
	v_mul_f32_e32 v54, 0x42000000, v54
	v_mul_f32_e32 v55, 0x42000000, v55
	v_mul_f32_e32 v56, 0x42000000, v56
	v_mul_f32_e32 v57, 0x42000000, v57
	v_mul_f32_e32 v58, 0x42000000, v58
	v_mul_f32_e32 v59, 0x42000000, v59
	v_mul_f32_e32 v60, 0x42000000, v60
	v_mul_f32_e32 v61, 0x42000000, v61
	v_mul_f32_e32 v62, 0x42000000, v62
	v_mul_f32_e32 v63, 0x42000000, v63
	v_mul_f32_e32 v64, 0x42000000, v64
	v_mul_f32_e32 v65, 0x42000000, v65
	v_cvt_pk_fp8_f32 v158, v50, v51
	v_cvt_pk_fp8_f32 v159, v54, v55
	v_cvt_pk_fp8_f32 v160, v58, v59
	v_cvt_pk_fp8_f32 v161, v62, v63
	v_cvt_pk_fp8_f32 v158, v52, v53 op_sel:[0,0,1]
	v_cvt_pk_fp8_f32 v159, v56, v57 op_sel:[0,0,1]
	v_cvt_pk_fp8_f32 v160, v60, v61 op_sel:[0,0,1]
	v_cvt_pk_fp8_f32 v161, v64, v65 op_sel:[0,0,1]
	global_load_dword v82, v178, s[100:101] nt
	s_add_u32 s100, s100, s89
	s_addc_u32 s101, s101, 0
	global_load_dword v83, v178, s[100:101] nt
	s_add_u32 s100, s100, s89
	s_addc_u32 s101, s101, 0
	global_load_dword v84, v178, s[100:101] nt
	s_add_u32 s100, s100, s89
	s_addc_u32 s101, s101, 0
	global_load_dword v85, v178, s[100:101] nt
	s_add_u32 s100, s100, s89
	s_addc_u32 s101, s101, 0
	global_load_dword v86, v178, s[100:101] nt
	s_add_u32 s100, s100, s89
	s_addc_u32 s101, s101, 0
	global_load_dword v87, v178, s[100:101] nt
	s_add_u32 s100, s100, s89
	s_addc_u32 s101, s101, 0
	global_load_dword v88, v178, s[100:101] nt
	s_add_u32 s100, s100, s89
	s_addc_u32 s101, s101, 0
	global_load_dword v89, v178, s[100:101] nt
	s_add_u32 s100, s100, s89
	s_addc_u32 s101, s101, 0
	global_load_dword v90, v178, s[100:101] nt
	s_add_u32 s100, s100, s89
	s_addc_u32 s101, s101, 0
	global_load_dword v91, v178, s[100:101] nt
	s_add_u32 s100, s100, s89
	s_addc_u32 s101, s101, 0
	global_load_dword v92, v178, s[100:101] nt
	s_add_u32 s100, s100, s89
	s_addc_u32 s101, s101, 0
	global_load_dword v93, v178, s[100:101] nt
	s_add_u32 s100, s100, s89
	s_addc_u32 s101, s101, 0
	global_load_dword v94, v178, s[100:101] nt
	s_add_u32 s100, s100, s89
	s_addc_u32 s101, s101, 0
	global_load_dword v95, v178, s[100:101] nt
	s_add_u32 s100, s100, s89
	s_addc_u32 s101, s101, 0
	global_load_dword v96, v178, s[100:101] nt
	s_add_u32 s100, s100, s89
	s_addc_u32 s101, s101, 0
	global_load_dword v97, v178, s[100:101] nt
	s_add_u32 s100, s100, s89
	s_addc_u32 s101, s101, 0
	s_waitcnt vmcnt(16)
	v_mul_f32_e32 v66, 0x42000000, v66
	v_mul_f32_e32 v67, 0x42000000, v67
	v_mul_f32_e32 v68, 0x42000000, v68
	v_mul_f32_e32 v69, 0x42000000, v69
	v_mul_f32_e32 v70, 0x42000000, v70
	v_mul_f32_e32 v71, 0x42000000, v71
	v_mul_f32_e32 v72, 0x42000000, v72
	v_mul_f32_e32 v73, 0x42000000, v73
	v_mul_f32_e32 v74, 0x42000000, v74
	v_mul_f32_e32 v75, 0x42000000, v75
	v_mul_f32_e32 v76, 0x42000000, v76
	v_mul_f32_e32 v77, 0x42000000, v77
	v_mul_f32_e32 v78, 0x42000000, v78
	v_mul_f32_e32 v79, 0x42000000, v79
	v_mul_f32_e32 v80, 0x42000000, v80
	v_mul_f32_e32 v81, 0x42000000, v81
	v_cvt_pk_fp8_f32 v162, v66, v67
	v_cvt_pk_fp8_f32 v163, v70, v71
	v_cvt_pk_fp8_f32 v164, v74, v75
	v_cvt_pk_fp8_f32 v165, v78, v79
	v_cvt_pk_fp8_f32 v162, v68, v69 op_sel:[0,0,1]
	v_cvt_pk_fp8_f32 v163, v72, v73 op_sel:[0,0,1]
	v_cvt_pk_fp8_f32 v164, v76, v77 op_sel:[0,0,1]
	v_cvt_pk_fp8_f32 v165, v80, v81 op_sel:[0,0,1]
	s_waitcnt vmcnt(0)
	v_mul_f32_e32 v82, 0x42000000, v82
	v_mul_f32_e32 v83, 0x42000000, v83
	v_mul_f32_e32 v84, 0x42000000, v84
	v_mul_f32_e32 v85, 0x42000000, v85
	v_mul_f32_e32 v86, 0x42000000, v86
	v_mul_f32_e32 v87, 0x42000000, v87
	v_mul_f32_e32 v88, 0x42000000, v88
	v_mul_f32_e32 v89, 0x42000000, v89
	v_mul_f32_e32 v90, 0x42000000, v90
	v_mul_f32_e32 v91, 0x42000000, v91
	v_mul_f32_e32 v92, 0x42000000, v92
	v_mul_f32_e32 v93, 0x42000000, v93
	v_mul_f32_e32 v94, 0x42000000, v94
	v_mul_f32_e32 v95, 0x42000000, v95
	v_mul_f32_e32 v96, 0x42000000, v96
	v_mul_f32_e32 v97, 0x42000000, v97
	v_cvt_pk_fp8_f32 v166, v82, v83
	v_cvt_pk_fp8_f32 v167, v86, v87
	v_cvt_pk_fp8_f32 v168, v90, v91
	v_cvt_pk_fp8_f32 v169, v94, v95
	v_cvt_pk_fp8_f32 v166, v84, v85 op_sel:[0,0,1]
	v_cvt_pk_fp8_f32 v167, v88, v89 op_sel:[0,0,1]
	v_cvt_pk_fp8_f32 v168, v92, v93 op_sel:[0,0,1]
	v_cvt_pk_fp8_f32 v169, v96, v97 op_sel:[0,0,1]
	s_mov_b32 vcc_lo, 0xaaaaaaaa
	s_mov_b32 vcc_hi, 0xaaaaaaaa
	s_nop 1
	v_cndmask_b32_dpp v170, v154, v158, vcc quad_perm:[1,0,3,2] row_mask:0xf bank_mask:0xf
	v_cndmask_b32_dpp v174, v162, v166, vcc quad_perm:[1,0,3,2] row_mask:0xf bank_mask:0xf
	v_cndmask_b32_dpp v171, v155, v159, vcc quad_perm:[1,0,3,2] row_mask:0xf bank_mask:0xf
	v_cndmask_b32_dpp v175, v163, v167, vcc quad_perm:[1,0,3,2] row_mask:0xf bank_mask:0xf
	v_cndmask_b32_dpp v172, v156, v160, vcc quad_perm:[1,0,3,2] row_mask:0xf bank_mask:0xf
	v_cndmask_b32_dpp v176, v164, v168, vcc quad_perm:[1,0,3,2] row_mask:0xf bank_mask:0xf
	v_cndmask_b32_dpp v173, v157, v161, vcc quad_perm:[1,0,3,2] row_mask:0xf bank_mask:0xf
	v_cndmask_b32_dpp v177, v165, v169, vcc quad_perm:[1,0,3,2] row_mask:0xf bank_mask:0xf
	s_mov_b32 vcc_lo, 0x55555555
	s_mov_b32 vcc_hi, 0x55555555
	s_nop 1
	v_cndmask_b32_dpp v154, v158, v154, vcc quad_perm:[1,0,3,2] row_mask:0xf bank_mask:0xf
	v_cndmask_b32_dpp v162, v166, v162, vcc quad_perm:[1,0,3,2] row_mask:0xf bank_mask:0xf
	v_cndmask_b32_dpp v155, v159, v155, vcc quad_perm:[1,0,3,2] row_mask:0xf bank_mask:0xf
	v_cndmask_b32_dpp v163, v167, v163, vcc quad_perm:[1,0,3,2] row_mask:0xf bank_mask:0xf
	v_cndmask_b32_dpp v156, v160, v156, vcc quad_perm:[1,0,3,2] row_mask:0xf bank_mask:0xf
	v_cndmask_b32_dpp v164, v168, v164, vcc quad_perm:[1,0,3,2] row_mask:0xf bank_mask:0xf
	v_cndmask_b32_dpp v157, v161, v157, vcc quad_perm:[1,0,3,2] row_mask:0xf bank_mask:0xf
	v_cndmask_b32_dpp v165, v169, v165, vcc quad_perm:[1,0,3,2] row_mask:0xf bank_mask:0xf
	s_mov_b32 vcc_lo, 0xcccccccc
	s_mov_b32 vcc_hi, 0xcccccccc
	s_nop 1
	v_cndmask_b32_dpp v158, v154, v162, vcc quad_perm:[2,3,0,1] row_mask:0xf bank_mask:0xf
	v_cndmask_b32_dpp v166, v170, v174, vcc quad_perm:[2,3,0,1] row_mask:0xf bank_mask:0xf
	v_cndmask_b32_dpp v159, v155, v163, vcc quad_perm:[2,3,0,1] row_mask:0xf bank_mask:0xf
	v_cndmask_b32_dpp v167, v171, v175, vcc quad_perm:[2,3,0,1] row_mask:0xf bank_mask:0xf
	v_cndmask_b32_dpp v160, v156, v164, vcc quad_perm:[2,3,0,1] row_mask:0xf bank_mask:0xf
	v_cndmask_b32_dpp v168, v172, v176, vcc quad_perm:[2,3,0,1] row_mask:0xf bank_mask:0xf
	v_cndmask_b32_dpp v161, v157, v165, vcc quad_perm:[2,3,0,1] row_mask:0xf bank_mask:0xf
	v_cndmask_b32_dpp v169, v173, v177, vcc quad_perm:[2,3,0,1] row_mask:0xf bank_mask:0xf
	s_mov_b32 vcc_lo, 0x33333333
	s_mov_b32 vcc_hi, 0x33333333
	s_nop 1
	v_cndmask_b32_dpp v154, v162, v154, vcc quad_perm:[2,3,0,1] row_mask:0xf bank_mask:0xf
	v_cndmask_b32_dpp v170, v174, v170, vcc quad_perm:[2,3,0,1] row_mask:0xf bank_mask:0xf
	v_cndmask_b32_dpp v155, v163, v155, vcc quad_perm:[2,3,0,1] row_mask:0xf bank_mask:0xf
	v_cndmask_b32_dpp v171, v175, v171, vcc quad_perm:[2,3,0,1] row_mask:0xf bank_mask:0xf
	v_cndmask_b32_dpp v156, v164, v156, vcc quad_perm:[2,3,0,1] row_mask:0xf bank_mask:0xf
	v_cndmask_b32_dpp v172, v176, v172, vcc quad_perm:[2,3,0,1] row_mask:0xf bank_mask:0xf
	v_cndmask_b32_dpp v157, v165, v157, vcc quad_perm:[2,3,0,1] row_mask:0xf bank_mask:0xf
	v_cndmask_b32_dpp v173, v177, v173, vcc quad_perm:[2,3,0,1] row_mask:0xf bank_mask:0xf
	global_store_dwordx4 v179, v[154:157], s[82:83] nt
	global_store_dwordx4 v180, v[170:173], s[82:83] nt
	global_store_dwordx4 v181, v[158:161], s[82:83] nt
	global_store_dwordx4 v190, v[166:169], s[82:83] nt
	v_readlane_b32 s2, v239, 0
	s_lshr_b32 s2, s2, 6
	s_add_i32 s2, s2, 6
	s_cmp_gt_u32 s2, 13
	s_cbranch_scc1 .Lhw_seam2_done
	s_add_i32 s2, s2, 28
	s_mul_i32 s2, s2, s74
	v_readlane_b32 s9, v239, 23
	s_lshr_b32 s9, s9, 3
	s_add_i32 s2, s2, s9
	s_cmp_gt_u32 s2, 24575
	s_cbranch_scc1 .Lhw_seam2_done
	v_mbcnt_lo_u32_b32 v178, -1, 0
	v_mbcnt_hi_u32_b32 v178, -1, v178
	v_and_b32_e32 v179, 60, v178
	v_lshlrev_b32_e32 v179, 10, v179
	v_and_b32_e32 v180, 3, v178
	v_lshl_or_b32 v179, v180, 4, v179
	v_add_u32_e32 v180, 0x400, v179
	v_add_u32_e32 v181, 0x800, v179
	v_add_u32_e32 v190, 0xc00, v179
	v_lshlrev_b32_e32 v178, 2, v178
	s_cmp_lt_u32 s2, 16384
	s_cbranch_scc0 .Lhw_dn_s2_1
	s_lshr_b32 s9, s2, 9
	s_bfe_u32 s32, s2, 0x40005
	s_and_b32 s53, s2, 31
	s_lshl_b32 s69, s9, 23
	s_lshl_b32 s100, s32, 19
	s_add_i32 s69, s69, s100
	s_lshl_b32 s100, s53, 8
	s_add_i32 s69, s69, s100
	s_lshl_b32 s98, s9, 11
	s_bfe_u32 s100, s53, 0x30001
	s_lshl_b32 s100, s100, 8
	s_add_i32 s98, s98, s100
	s_lshr_b32 s100, s53, 4
	s_lshl_b32 s100, s100, 7
	s_add_i32 s98, s98, s100
	s_and_b32 s100, s53, 1
	s_lshl_b32 s100, s100, 6
	s_add_i32 s98, s98, s100
	s_lshl_b32 s98, s98, 10
	s_lshl_b32 s100, s32, 6
	s_add_i32 s98, s98, s100
	s_add_i32 s98, s98, 0x2000000
	v_readlane_b32 s82, v239, 11
	v_readlane_b32 s83, v239, 12
	s_movk_i32 s89, 8192
	s_branch .Lhw_go_s2_1

.Lhw_go_s3_0:
	s_add_u32 s100, s82, s69
	s_addc_u32 s101, s83, 0
	v_readlane_b32 s82, v239, 44
	v_readlane_b32 s83, v239, 45
	s_add_u32 s82, s82, s98
	s_addc_u32 s83, s83, 0
	global_load_dword v34, v178, s[100:101] nt
	s_add_u32 s100, s100, s89
	s_addc_u32 s101, s101, 0
	global_load_dword v35, v178, s[100:101] nt
	s_add_u32 s100, s100, s89
	s_addc_u32 s101, s101, 0
	global_load_dword v36, v178, s[100:101] nt
	s_add_u32 s100, s100, s89
	s_addc_u32 s101, s101, 0
	global_load_dword v37, v178, s[100:101] nt
	s_add_u32 s100, s100, s89
	s_addc_u32 s101, s101, 0
	global_load_dword v38, v178, s[100:101] nt
	s_add_u32 s100, s100, s89
	s_addc_u32 s101, s101, 0
	global_load_dword v39, v178, s[100:101] nt
	s_add_u32 s100, s100, s89
	s_addc_u32 s101, s101, 0
	global_load_dword v40, v178, s[100:101] nt
	s_add_u32 s100, s100, s89
	s_addc_u32 s101, s101, 0
	global_load_dword v41, v178, s[100:101] nt
	s_add_u32 s100, s100, s89
	s_addc_u32 s101, s101, 0
	global_load_dword v42, v178, s[100:101] nt
	s_add_u32 s100, s100, s89
	s_addc_u32 s101, s101, 0
	global_load_dword v43, v178, s[100:101] nt
	s_add_u32 s100, s100, s89
	s_addc_u32 s101, s101, 0
	global_load_dword v44, v178, s[100:101] nt
	s_add_u32 s100, s100, s89
	s_addc_u32 s101, s101, 0
	global_load_dword v45, v178, s[100:101] nt
	s_add_u32 s100, s100, s89
	s_addc_u32 s101, s101, 0
	global_load_dword v46, v178, s[100:101] nt
	s_add_u32 s100, s100, s89
	s_addc_u32 s101, s101, 0
	global_load_dword v47, v178, s[100:101] nt
	s_add_u32 s100, s100, s89
	s_addc_u32 s101, s101, 0
	global_load_dword v48, v178, s[100:101] nt
	s_add_u32 s100, s100, s89
	s_addc_u32 s101, s101, 0
	global_load_dword v49, v178, s[100:101] nt
	s_add_u32 s100, s100, s89
	s_addc_u32 s101, s101, 0
	global_load_dword v50, v178, s[100:101] nt
	s_add_u32 s100, s100, s89
	s_addc_u32 s101, s101, 0
	global_load_dword v51, v178, s[100:101] nt
	s_add_u32 s100, s100, s89
	s_addc_u32 s101, s101, 0
	global_load_dword v52, v178, s[100:101] nt
	s_add_u32 s100, s100, s89
	s_addc_u32 s101, s101, 0
	global_load_dword v53, v178, s[100:101] nt
	s_add_u32 s100, s100, s89
	s_addc_u32 s101, s101, 0
	global_load_dword v54, v178, s[100:101] nt
	s_add_u32 s100, s100, s89
	s_addc_u32 s101, s101, 0
	global_load_dword v55, v178, s[100:101] nt
	s_add_u32 s100, s100, s89
	s_addc_u32 s101, s101, 0
	global_load_dword v56, v178, s[100:101] nt
	s_add_u32 s100, s100, s89
	s_addc_u32 s101, s101, 0
	global_load_dword v57, v178, s[100:101] nt
	s_add_u32 s100, s100, s89
	s_addc_u32 s101, s101, 0
	global_load_dword v58, v178, s[100:101] nt
	s_add_u32 s100, s100, s89
	s_addc_u32 s101, s101, 0
	global_load_dword v59, v178, s[100:101] nt
	s_add_u32 s100, s100, s89
	s_addc_u32 s101, s101, 0
	global_load_dword v60, v178, s[100:101] nt
	s_add_u32 s100, s100, s89
	s_addc_u32 s101, s101, 0
	global_load_dword v61, v178, s[100:101] nt
	s_add_u32 s100, s100, s89
	s_addc_u32 s101, s101, 0
	global_load_dword v62, v178, s[100:101] nt
	s_add_u32 s100, s100, s89
	s_addc_u32 s101, s101, 0
	global_load_dword v63, v178, s[100:101] nt
	s_add_u32 s100, s100, s89
	s_addc_u32 s101, s101, 0
	global_load_dword v64, v178, s[100:101] nt
	s_add_u32 s100, s100, s89
	s_addc_u32 s101, s101, 0
	global_load_dword v65, v178, s[100:101] nt
	s_add_u32 s100, s100, s89
	s_addc_u32 s101, s101, 0
	s_waitcnt vmcnt(16)
	v_mul_f32_e32 v34, 0x42000000, v34
	v_mul_f32_e32 v35, 0x42000000, v35
	v_mul_f32_e32 v36, 0x42000000, v36
	v_mul_f32_e32 v37, 0x42000000, v37
	v_mul_f32_e32 v38, 0x42000000, v38
	v_mul_f32_e32 v39, 0x42000000, v39
	v_mul_f32_e32 v40, 0x42000000, v40
	v_mul_f32_e32 v41, 0x42000000, v41
	v_mul_f32_e32 v42, 0x42000000, v42
	v_mul_f32_e32 v43, 0x42000000, v43
	v_mul_f32_e32 v44, 0x42000000, v44
	v_mul_f32_e32 v45, 0x42000000, v45
	v_mul_f32_e32 v46, 0x42000000, v46
	v_mul_f32_e32 v47, 0x42000000, v47
	v_mul_f32_e32 v48, 0x42000000, v48
	v_mul_f32_e32 v49, 0x42000000, v49
	v_cvt_pk_fp8_f32 v154, v34, v35
	v_cvt_pk_fp8_f32 v155, v38, v39
	v_cvt_pk_fp8_f32 v156, v42, v43
	v_cvt_pk_fp8_f32 v157, v46, v47
	v_cvt_pk_fp8_f32 v154, v36, v37 op_sel:[0,0,1]
	v_cvt_pk_fp8_f32 v155, v40, v41 op_sel:[0,0,1]
	v_cvt_pk_fp8_f32 v156, v44, v45 op_sel:[0,0,1]
	v_cvt_pk_fp8_f32 v157, v48, v49 op_sel:[0,0,1]
	global_load_dword v66, v178, s[100:101] nt
	s_add_u32 s100, s100, s89
	s_addc_u32 s101, s101, 0
	global_load_dword v67, v178, s[100:101] nt
	s_add_u32 s100, s100, s89
	s_addc_u32 s101, s101, 0
	global_load_dword v68, v178, s[100:101] nt
	s_add_u32 s100, s100, s89
	s_addc_u32 s101, s101, 0
	global_load_dword v69, v178, s[100:101] nt
	s_add_u32 s100, s100, s89
	s_addc_u32 s101, s101, 0
	global_load_dword v70, v178, s[100:101] nt
	s_add_u32 s100, s100, s89
	s_addc_u32 s101, s101, 0
	global_load_dword v71, v178, s[100:101] nt
	s_add_u32 s100, s100, s89
	s_addc_u32 s101, s101, 0
	global_load_dword v72, v178, s[100:101] nt
	s_add_u32 s100, s100, s89
	s_addc_u32 s101, s101, 0
	global_load_dword v73, v178, s[100:101] nt
	s_add_u32 s100, s100, s89
	s_addc_u32 s101, s101, 0
	global_load_dword v74, v178, s[100:101] nt
	s_add_u32 s100, s100, s89
	s_addc_u32 s101, s101, 0
	global_load_dword v75, v178, s[100:101] nt
	s_add_u32 s100, s100, s89
	s_addc_u32 s101, s101, 0
	global_load_dword v76, v178, s[100:101] nt
	s_add_u32 s100, s100, s89
	s_addc_u32 s101, s101, 0
	global_load_dword v77, v178, s[100:101] nt
	s_add_u32 s100, s100, s89
	s_addc_u32 s101, s101, 0
	global_load_dword v78, v178, s[100:101] nt
	s_add_u32 s100, s100, s89
	s_addc_u32 s101, s101, 0
	global_load_dword v79, v178, s[100:101] nt
	s_add_u32 s100, s100, s89
	s_addc_u32 s101, s101, 0
	global_load_dword v80, v178, s[100:101] nt
	s_add_u32 s100, s100, s89
	s_addc_u32 s101, s101, 0
	global_load_dword v81, v178, s[100:101] nt
	s_add_u32 s100, s100, s89
	s_addc_u32 s101, s101, 0
	s_waitcnt vmcnt(16)
	v_mul_f32_e32 v50, 0x42000000, v50
	v_mul_f32_e32 v51, 0x42000000, v51
	v_mul_f32_e32 v52, 0x42000000, v52
	v_mul_f32_e32 v53, 0x42000000, v53
	v_mul_f32_e32 v54, 0x42000000, v54
	v_mul_f32_e32 v55, 0x42000000, v55
	v_mul_f32_e32 v56, 0x42000000, v56
	v_mul_f32_e32 v57, 0x42000000, v57
	v_mul_f32_e32 v58, 0x42000000, v58
	v_mul_f32_e32 v59, 0x42000000, v59
	v_mul_f32_e32 v60, 0x42000000, v60
	v_mul_f32_e32 v61, 0x42000000, v61
	v_mul_f32_e32 v62, 0x42000000, v62
	v_mul_f32_e32 v63, 0x42000000, v63
	v_mul_f32_e32 v64, 0x42000000, v64
	v_mul_f32_e32 v65, 0x42000000, v65
	v_cvt_pk_fp8_f32 v158, v50, v51
	v_cvt_pk_fp8_f32 v159, v54, v55
	v_cvt_pk_fp8_f32 v160, v58, v59
	v_cvt_pk_fp8_f32 v161, v62, v63
	v_cvt_pk_fp8_f32 v158, v52, v53 op_sel:[0,0,1]
	v_cvt_pk_fp8_f32 v159, v56, v57 op_sel:[0,0,1]
	v_cvt_pk_fp8_f32 v160, v60, v61 op_sel:[0,0,1]
	v_cvt_pk_fp8_f32 v161, v64, v65 op_sel:[0,0,1]
	global_load_dword v82, v178, s[100:101] nt
	s_add_u32 s100, s100, s89
	s_addc_u32 s101, s101, 0
	global_load_dword v83, v178, s[100:101] nt
	s_add_u32 s100, s100, s89
	s_addc_u32 s101, s101, 0
	global_load_dword v84, v178, s[100:101] nt
	s_add_u32 s100, s100, s89
	s_addc_u32 s101, s101, 0
	global_load_dword v85, v178, s[100:101] nt
	s_add_u32 s100, s100, s89
	s_addc_u32 s101, s101, 0
	global_load_dword v86, v178, s[100:101] nt
	s_add_u32 s100, s100, s89
	s_addc_u32 s101, s101, 0
	global_load_dword v87, v178, s[100:101] nt
	s_add_u32 s100, s100, s89
	s_addc_u32 s101, s101, 0
	global_load_dword v88, v178, s[100:101] nt
	s_add_u32 s100, s100, s89
	s_addc_u32 s101, s101, 0
	global_load_dword v89, v178, s[100:101] nt
	s_add_u32 s100, s100, s89
	s_addc_u32 s101, s101, 0
	global_load_dword v90, v178, s[100:101] nt
	s_add_u32 s100, s100, s89
	s_addc_u32 s101, s101, 0
	global_load_dword v91, v178, s[100:101] nt
	s_add_u32 s100, s100, s89
	s_addc_u32 s101, s101, 0
	global_load_dword v92, v178, s[100:101] nt
	s_add_u32 s100, s100, s89
	s_addc_u32 s101, s101, 0
	global_load_dword v93, v178, s[100:101] nt
	s_add_u32 s100, s100, s89
	s_addc_u32 s101, s101, 0
	global_load_dword v94, v178, s[100:101] nt
	s_add_u32 s100, s100, s89
	s_addc_u32 s101, s101, 0
	global_load_dword v95, v178, s[100:101] nt
	s_add_u32 s100, s100, s89
	s_addc_u32 s101, s101, 0
	global_load_dword v96, v178, s[100:101] nt
	s_add_u32 s100, s100, s89
	s_addc_u32 s101, s101, 0
	global_load_dword v97, v178, s[100:101] nt
	s_add_u32 s100, s100, s89
	s_addc_u32 s101, s101, 0
	s_waitcnt vmcnt(16)
	v_mul_f32_e32 v66, 0x42000000, v66
	v_mul_f32_e32 v67, 0x42000000, v67
	v_mul_f32_e32 v68, 0x42000000, v68
	v_mul_f32_e32 v69, 0x42000000, v69
	v_mul_f32_e32 v70, 0x42000000, v70
	v_mul_f32_e32 v71, 0x42000000, v71
	v_mul_f32_e32 v72, 0x42000000, v72
	v_mul_f32_e32 v73, 0x42000000, v73
	v_mul_f32_e32 v74, 0x42000000, v74
	v_mul_f32_e32 v75, 0x42000000, v75
	v_mul_f32_e32 v76, 0x42000000, v76
	v_mul_f32_e32 v77, 0x42000000, v77
	v_mul_f32_e32 v78, 0x42000000, v78
	v_mul_f32_e32 v79, 0x42000000, v79
	v_mul_f32_e32 v80, 0x42000000, v80
	v_mul_f32_e32 v81, 0x42000000, v81
	v_cvt_pk_fp8_f32 v162, v66, v67
	v_cvt_pk_fp8_f32 v163, v70, v71
	v_cvt_pk_fp8_f32 v164, v74, v75
	v_cvt_pk_fp8_f32 v165, v78, v79
	v_cvt_pk_fp8_f32 v162, v68, v69 op_sel:[0,0,1]
	v_cvt_pk_fp8_f32 v163, v72, v73 op_sel:[0,0,1]
	v_cvt_pk_fp8_f32 v164, v76, v77 op_sel:[0,0,1]
	v_cvt_pk_fp8_f32 v165, v80, v81 op_sel:[0,0,1]
	s_waitcnt vmcnt(0)
	v_mul_f32_e32 v82, 0x42000000, v82
	v_mul_f32_e32 v83, 0x42000000, v83
	v_mul_f32_e32 v84, 0x42000000, v84
	v_mul_f32_e32 v85, 0x42000000, v85
	v_mul_f32_e32 v86, 0x42000000, v86
	v_mul_f32_e32 v87, 0x42000000, v87
	v_mul_f32_e32 v88, 0x42000000, v88
	v_mul_f32_e32 v89, 0x42000000, v89
	v_mul_f32_e32 v90, 0x42000000, v90
	v_mul_f32_e32 v91, 0x42000000, v91
	v_mul_f32_e32 v92, 0x42000000, v92
	v_mul_f32_e32 v93, 0x42000000, v93
	v_mul_f32_e32 v94, 0x42000000, v94
	v_mul_f32_e32 v95, 0x42000000, v95
	v_mul_f32_e32 v96, 0x42000000, v96
	v_mul_f32_e32 v97, 0x42000000, v97
	v_cvt_pk_fp8_f32 v166, v82, v83
	v_cvt_pk_fp8_f32 v167, v86, v87
	v_cvt_pk_fp8_f32 v168, v90, v91
	v_cvt_pk_fp8_f32 v169, v94, v95
	v_cvt_pk_fp8_f32 v166, v84, v85 op_sel:[0,0,1]
	v_cvt_pk_fp8_f32 v167, v88, v89 op_sel:[0,0,1]
	v_cvt_pk_fp8_f32 v168, v92, v93 op_sel:[0,0,1]
	v_cvt_pk_fp8_f32 v169, v96, v97 op_sel:[0,0,1]
	s_mov_b32 vcc_lo, 0xaaaaaaaa
	s_mov_b32 vcc_hi, 0xaaaaaaaa
	s_nop 1
	v_cndmask_b32_dpp v170, v154, v158, vcc quad_perm:[1,0,3,2] row_mask:0xf bank_mask:0xf
	v_cndmask_b32_dpp v174, v162, v166, vcc quad_perm:[1,0,3,2] row_mask:0xf bank_mask:0xf
	v_cndmask_b32_dpp v171, v155, v159, vcc quad_perm:[1,0,3,2] row_mask:0xf bank_mask:0xf
	v_cndmask_b32_dpp v175, v163, v167, vcc quad_perm:[1,0,3,2] row_mask:0xf bank_mask:0xf
	v_cndmask_b32_dpp v172, v156, v160, vcc quad_perm:[1,0,3,2] row_mask:0xf bank_mask:0xf
	v_cndmask_b32_dpp v176, v164, v168, vcc quad_perm:[1,0,3,2] row_mask:0xf bank_mask:0xf
	v_cndmask_b32_dpp v173, v157, v161, vcc quad_perm:[1,0,3,2] row_mask:0xf bank_mask:0xf
	v_cndmask_b32_dpp v177, v165, v169, vcc quad_perm:[1,0,3,2] row_mask:0xf bank_mask:0xf
	s_mov_b32 vcc_lo, 0x55555555
	s_mov_b32 vcc_hi, 0x55555555
	s_nop 1
	v_cndmask_b32_dpp v154, v158, v154, vcc quad_perm:[1,0,3,2] row_mask:0xf bank_mask:0xf
	v_cndmask_b32_dpp v162, v166, v162, vcc quad_perm:[1,0,3,2] row_mask:0xf bank_mask:0xf
	v_cndmask_b32_dpp v155, v159, v155, vcc quad_perm:[1,0,3,2] row_mask:0xf bank_mask:0xf
	v_cndmask_b32_dpp v163, v167, v163, vcc quad_perm:[1,0,3,2] row_mask:0xf bank_mask:0xf
	v_cndmask_b32_dpp v156, v160, v156, vcc quad_perm:[1,0,3,2] row_mask:0xf bank_mask:0xf
	v_cndmask_b32_dpp v164, v168, v164, vcc quad_perm:[1,0,3,2] row_mask:0xf bank_mask:0xf
	v_cndmask_b32_dpp v157, v161, v157, vcc quad_perm:[1,0,3,2] row_mask:0xf bank_mask:0xf
	v_cndmask_b32_dpp v165, v169, v165, vcc quad_perm:[1,0,3,2] row_mask:0xf bank_mask:0xf
	s_mov_b32 vcc_lo, 0xcccccccc
	s_mov_b32 vcc_hi, 0xcccccccc
	s_nop 1
	v_cndmask_b32_dpp v158, v154, v162, vcc quad_perm:[2,3,0,1] row_mask:0xf bank_mask:0xf
	v_cndmask_b32_dpp v166, v170, v174, vcc quad_perm:[2,3,0,1] row_mask:0xf bank_mask:0xf
	v_cndmask_b32_dpp v159, v155, v163, vcc quad_perm:[2,3,0,1] row_mask:0xf bank_mask:0xf
	v_cndmask_b32_dpp v167, v171, v175, vcc quad_perm:[2,3,0,1] row_mask:0xf bank_mask:0xf
	v_cndmask_b32_dpp v160, v156, v164, vcc quad_perm:[2,3,0,1] row_mask:0xf bank_mask:0xf
	v_cndmask_b32_dpp v168, v172, v176, vcc quad_perm:[2,3,0,1] row_mask:0xf bank_mask:0xf
	v_cndmask_b32_dpp v161, v157, v165, vcc quad_perm:[2,3,0,1] row_mask:0xf bank_mask:0xf
	v_cndmask_b32_dpp v169, v173, v177, vcc quad_perm:[2,3,0,1] row_mask:0xf bank_mask:0xf
	s_mov_b32 vcc_lo, 0x33333333
	s_mov_b32 vcc_hi, 0x33333333
	s_nop 1
	v_cndmask_b32_dpp v154, v162, v154, vcc quad_perm:[2,3,0,1] row_mask:0xf bank_mask:0xf
	v_cndmask_b32_dpp v170, v174, v170, vcc quad_perm:[2,3,0,1] row_mask:0xf bank_mask:0xf
	v_cndmask_b32_dpp v155, v163, v155, vcc quad_perm:[2,3,0,1] row_mask:0xf bank_mask:0xf
	v_cndmask_b32_dpp v171, v175, v171, vcc quad_perm:[2,3,0,1] row_mask:0xf bank_mask:0xf
	v_cndmask_b32_dpp v156, v164, v156, vcc quad_perm:[2,3,0,1] row_mask:0xf bank_mask:0xf
	v_cndmask_b32_dpp v172, v176, v172, vcc quad_perm:[2,3,0,1] row_mask:0xf bank_mask:0xf
	v_cndmask_b32_dpp v157, v165, v157, vcc quad_perm:[2,3,0,1] row_mask:0xf bank_mask:0xf
	v_cndmask_b32_dpp v173, v177, v173, vcc quad_perm:[2,3,0,1] row_mask:0xf bank_mask:0xf
	global_store_dwordx4 v179, v[154:157], s[82:83] nt
	global_store_dwordx4 v180, v[170:173], s[82:83] nt
	global_store_dwordx4 v181, v[158:161], s[82:83] nt
	global_store_dwordx4 v190, v[166:169], s[82:83] nt
	v_readlane_b32 s2, v239, 0
	s_lshr_b32 s2, s2, 6
	s_add_i32 s2, s2, 6
	s_cmp_gt_u32 s2, 13
	s_cbranch_scc1 .Lhw_seam3_done
	s_add_i32 s2, s2, 42
	s_mul_i32 s2, s2, s74
	v_readlane_b32 s9, v239, 23
	s_lshr_b32 s9, s9, 3
	s_add_i32 s2, s2, s9
	s_cmp_gt_u32 s2, 24575
	s_cbranch_scc1 .Lhw_seam3_done
	v_mbcnt_lo_u32_b32 v178, -1, 0
	v_mbcnt_hi_u32_b32 v178, -1, v178
	v_and_b32_e32 v179, 60, v178
	v_lshlrev_b32_e32 v179, 10, v179
	v_and_b32_e32 v180, 3, v178
	v_lshl_or_b32 v179, v180, 4, v179
	v_add_u32_e32 v180, 0x400, v179
	v_add_u32_e32 v181, 0x800, v179
	v_add_u32_e32 v190, 0xc00, v179
	v_lshlrev_b32_e32 v178, 2, v178
	s_cmp_lt_u32 s2, 16384
	s_cbranch_scc0 .Lhw_dn_s3_1
	s_lshr_b32 s9, s2, 9
	s_bfe_u32 s32, s2, 0x40005
	s_and_b32 s53, s2, 31
	s_lshl_b32 s69, s9, 23
	s_lshl_b32 s100, s32, 19
	s_add_i32 s69, s69, s100
	s_lshl_b32 s100, s53, 8
	s_add_i32 s69, s69, s100
	s_lshl_b32 s98, s9, 11
	s_bfe_u32 s100, s53, 0x30001
	s_lshl_b32 s100, s100, 8
	s_add_i32 s98, s98, s100
	s_lshr_b32 s100, s53, 4
	s_lshl_b32 s100, s100, 7
	s_add_i32 s98, s98, s100
	s_and_b32 s100, s53, 1
	s_lshl_b32 s100, s100, 6
	s_add_i32 s98, s98, s100
	s_lshl_b32 s98, s98, 10
	s_lshl_b32 s100, s32, 6
	s_add_i32 s98, s98, s100
	s_add_i32 s98, s98, 0x2000000
	v_readlane_b32 s82, v239, 11
	v_readlane_b32 s83, v239, 12
	s_movk_i32 s89, 8192
	s_branch .Lhw_go_s3_1

.Lhw_go_s4_0:
	s_add_u32 s100, s82, s69
	s_addc_u32 s101, s83, 0
	v_readlane_b32 s82, v239, 44
	v_readlane_b32 s83, v239, 45
	s_add_u32 s82, s82, s98
	s_addc_u32 s83, s83, 0
	global_load_dword v34, v178, s[100:101] nt
	s_add_u32 s100, s100, s89
	s_addc_u32 s101, s101, 0
	global_load_dword v35, v178, s[100:101] nt
	s_add_u32 s100, s100, s89
	s_addc_u32 s101, s101, 0
	global_load_dword v36, v178, s[100:101] nt
	s_add_u32 s100, s100, s89
	s_addc_u32 s101, s101, 0
	global_load_dword v37, v178, s[100:101] nt
	s_add_u32 s100, s100, s89
	s_addc_u32 s101, s101, 0
	global_load_dword v38, v178, s[100:101] nt
	s_add_u32 s100, s100, s89
	s_addc_u32 s101, s101, 0
	global_load_dword v39, v178, s[100:101] nt
	s_add_u32 s100, s100, s89
	s_addc_u32 s101, s101, 0
	global_load_dword v40, v178, s[100:101] nt
	s_add_u32 s100, s100, s89
	s_addc_u32 s101, s101, 0
	global_load_dword v41, v178, s[100:101] nt
	s_add_u32 s100, s100, s89
	s_addc_u32 s101, s101, 0
	global_load_dword v42, v178, s[100:101] nt
	s_add_u32 s100, s100, s89
	s_addc_u32 s101, s101, 0
	global_load_dword v43, v178, s[100:101] nt
	s_add_u32 s100, s100, s89
	s_addc_u32 s101, s101, 0
	global_load_dword v44, v178, s[100:101] nt
	s_add_u32 s100, s100, s89
	s_addc_u32 s101, s101, 0
	global_load_dword v45, v178, s[100:101] nt
	s_add_u32 s100, s100, s89
	s_addc_u32 s101, s101, 0
	global_load_dword v46, v178, s[100:101] nt
	s_add_u32 s100, s100, s89
	s_addc_u32 s101, s101, 0
	global_load_dword v47, v178, s[100:101] nt
	s_add_u32 s100, s100, s89
	s_addc_u32 s101, s101, 0
	global_load_dword v48, v178, s[100:101] nt
	s_add_u32 s100, s100, s89
	s_addc_u32 s101, s101, 0
	global_load_dword v49, v178, s[100:101] nt
	s_add_u32 s100, s100, s89
	s_addc_u32 s101, s101, 0
	global_load_dword v50, v178, s[100:101] nt
	s_add_u32 s100, s100, s89
	s_addc_u32 s101, s101, 0
	global_load_dword v51, v178, s[100:101] nt
	s_add_u32 s100, s100, s89
	s_addc_u32 s101, s101, 0
	global_load_dword v52, v178, s[100:101] nt
	s_add_u32 s100, s100, s89
	s_addc_u32 s101, s101, 0
	global_load_dword v53, v178, s[100:101] nt
	s_add_u32 s100, s100, s89
	s_addc_u32 s101, s101, 0
	global_load_dword v54, v178, s[100:101] nt
	s_add_u32 s100, s100, s89
	s_addc_u32 s101, s101, 0
	global_load_dword v55, v178, s[100:101] nt
	s_add_u32 s100, s100, s89
	s_addc_u32 s101, s101, 0
	global_load_dword v56, v178, s[100:101] nt
	s_add_u32 s100, s100, s89
	s_addc_u32 s101, s101, 0
	global_load_dword v57, v178, s[100:101] nt
	s_add_u32 s100, s100, s89
	s_addc_u32 s101, s101, 0
	global_load_dword v58, v178, s[100:101] nt
	s_add_u32 s100, s100, s89
	s_addc_u32 s101, s101, 0
	global_load_dword v59, v178, s[100:101] nt
	s_add_u32 s100, s100, s89
	s_addc_u32 s101, s101, 0
	global_load_dword v60, v178, s[100:101] nt
	s_add_u32 s100, s100, s89
	s_addc_u32 s101, s101, 0
	global_load_dword v61, v178, s[100:101] nt
	s_add_u32 s100, s100, s89
	s_addc_u32 s101, s101, 0
	global_load_dword v62, v178, s[100:101] nt
	s_add_u32 s100, s100, s89
	s_addc_u32 s101, s101, 0
	global_load_dword v63, v178, s[100:101] nt
	s_add_u32 s100, s100, s89
	s_addc_u32 s101, s101, 0
	global_load_dword v64, v178, s[100:101] nt
	s_add_u32 s100, s100, s89
	s_addc_u32 s101, s101, 0
	global_load_dword v65, v178, s[100:101] nt
	s_add_u32 s100, s100, s89
	s_addc_u32 s101, s101, 0
	s_waitcnt vmcnt(16)
	v_mul_f32_e32 v34, 0x42000000, v34
	v_mul_f32_e32 v35, 0x42000000, v35
	v_mul_f32_e32 v36, 0x42000000, v36
	v_mul_f32_e32 v37, 0x42000000, v37
	v_mul_f32_e32 v38, 0x42000000, v38
	v_mul_f32_e32 v39, 0x42000000, v39
	v_mul_f32_e32 v40, 0x42000000, v40
	v_mul_f32_e32 v41, 0x42000000, v41
	v_mul_f32_e32 v42, 0x42000000, v42
	v_mul_f32_e32 v43, 0x42000000, v43
	v_mul_f32_e32 v44, 0x42000000, v44
	v_mul_f32_e32 v45, 0x42000000, v45
	v_mul_f32_e32 v46, 0x42000000, v46
	v_mul_f32_e32 v47, 0x42000000, v47
	v_mul_f32_e32 v48, 0x42000000, v48
	v_mul_f32_e32 v49, 0x42000000, v49
	v_cvt_pk_fp8_f32 v154, v34, v35
	v_cvt_pk_fp8_f32 v155, v38, v39
	v_cvt_pk_fp8_f32 v156, v42, v43
	v_cvt_pk_fp8_f32 v157, v46, v47
	v_cvt_pk_fp8_f32 v154, v36, v37 op_sel:[0,0,1]
	v_cvt_pk_fp8_f32 v155, v40, v41 op_sel:[0,0,1]
	v_cvt_pk_fp8_f32 v156, v44, v45 op_sel:[0,0,1]
	v_cvt_pk_fp8_f32 v157, v48, v49 op_sel:[0,0,1]
	global_load_dword v66, v178, s[100:101] nt
	s_add_u32 s100, s100, s89
	s_addc_u32 s101, s101, 0
	global_load_dword v67, v178, s[100:101] nt
	s_add_u32 s100, s100, s89
	s_addc_u32 s101, s101, 0
	global_load_dword v68, v178, s[100:101] nt
	s_add_u32 s100, s100, s89
	s_addc_u32 s101, s101, 0
	global_load_dword v69, v178, s[100:101] nt
	s_add_u32 s100, s100, s89
	s_addc_u32 s101, s101, 0
	global_load_dword v70, v178, s[100:101] nt
	s_add_u32 s100, s100, s89
	s_addc_u32 s101, s101, 0
	global_load_dword v71, v178, s[100:101] nt
	s_add_u32 s100, s100, s89
	s_addc_u32 s101, s101, 0
	global_load_dword v72, v178, s[100:101] nt
	s_add_u32 s100, s100, s89
	s_addc_u32 s101, s101, 0
	global_load_dword v73, v178, s[100:101] nt
	s_add_u32 s100, s100, s89
	s_addc_u32 s101, s101, 0
	global_load_dword v74, v178, s[100:101] nt
	s_add_u32 s100, s100, s89
	s_addc_u32 s101, s101, 0
	global_load_dword v75, v178, s[100:101] nt
	s_add_u32 s100, s100, s89
	s_addc_u32 s101, s101, 0
	global_load_dword v76, v178, s[100:101] nt
	s_add_u32 s100, s100, s89
	s_addc_u32 s101, s101, 0
	global_load_dword v77, v178, s[100:101] nt
	s_add_u32 s100, s100, s89
	s_addc_u32 s101, s101, 0
	global_load_dword v78, v178, s[100:101] nt
	s_add_u32 s100, s100, s89
	s_addc_u32 s101, s101, 0
	global_load_dword v79, v178, s[100:101] nt
	s_add_u32 s100, s100, s89
	s_addc_u32 s101, s101, 0
	global_load_dword v80, v178, s[100:101] nt
	s_add_u32 s100, s100, s89
	s_addc_u32 s101, s101, 0
	global_load_dword v81, v178, s[100:101] nt
	s_add_u32 s100, s100, s89
	s_addc_u32 s101, s101, 0
	s_waitcnt vmcnt(16)
	v_mul_f32_e32 v50, 0x42000000, v50
	v_mul_f32_e32 v51, 0x42000000, v51
	v_mul_f32_e32 v52, 0x42000000, v52
	v_mul_f32_e32 v53, 0x42000000, v53
	v_mul_f32_e32 v54, 0x42000000, v54
	v_mul_f32_e32 v55, 0x42000000, v55
	v_mul_f32_e32 v56, 0x42000000, v56
	v_mul_f32_e32 v57, 0x42000000, v57
	v_mul_f32_e32 v58, 0x42000000, v58
	v_mul_f32_e32 v59, 0x42000000, v59
	v_mul_f32_e32 v60, 0x42000000, v60
	v_mul_f32_e32 v61, 0x42000000, v61
	v_mul_f32_e32 v62, 0x42000000, v62
	v_mul_f32_e32 v63, 0x42000000, v63
	v_mul_f32_e32 v64, 0x42000000, v64
	v_mul_f32_e32 v65, 0x42000000, v65
	v_cvt_pk_fp8_f32 v158, v50, v51
	v_cvt_pk_fp8_f32 v159, v54, v55
	v_cvt_pk_fp8_f32 v160, v58, v59
	v_cvt_pk_fp8_f32 v161, v62, v63
	v_cvt_pk_fp8_f32 v158, v52, v53 op_sel:[0,0,1]
	v_cvt_pk_fp8_f32 v159, v56, v57 op_sel:[0,0,1]
	v_cvt_pk_fp8_f32 v160, v60, v61 op_sel:[0,0,1]
	v_cvt_pk_fp8_f32 v161, v64, v65 op_sel:[0,0,1]
	global_load_dword v82, v178, s[100:101] nt
	s_add_u32 s100, s100, s89
	s_addc_u32 s101, s101, 0
	global_load_dword v83, v178, s[100:101] nt
	s_add_u32 s100, s100, s89
	s_addc_u32 s101, s101, 0
	global_load_dword v84, v178, s[100:101] nt
	s_add_u32 s100, s100, s89
	s_addc_u32 s101, s101, 0
	global_load_dword v85, v178, s[100:101] nt
	s_add_u32 s100, s100, s89
	s_addc_u32 s101, s101, 0
	global_load_dword v86, v178, s[100:101] nt
	s_add_u32 s100, s100, s89
	s_addc_u32 s101, s101, 0
	global_load_dword v87, v178, s[100:101] nt
	s_add_u32 s100, s100, s89
	s_addc_u32 s101, s101, 0
	global_load_dword v88, v178, s[100:101] nt
	s_add_u32 s100, s100, s89
	s_addc_u32 s101, s101, 0
	global_load_dword v89, v178, s[100:101] nt
	s_add_u32 s100, s100, s89
	s_addc_u32 s101, s101, 0
	global_load_dword v90, v178, s[100:101] nt
	s_add_u32 s100, s100, s89
	s_addc_u32 s101, s101, 0
	global_load_dword v91, v178, s[100:101] nt
	s_add_u32 s100, s100, s89
	s_addc_u32 s101, s101, 0
	global_load_dword v92, v178, s[100:101] nt
	s_add_u32 s100, s100, s89
	s_addc_u32 s101, s101, 0
	global_load_dword v93, v178, s[100:101] nt
	s_add_u32 s100, s100, s89
	s_addc_u32 s101, s101, 0
	global_load_dword v94, v178, s[100:101] nt
	s_add_u32 s100, s100, s89
	s_addc_u32 s101, s101, 0
	global_load_dword v95, v178, s[100:101] nt
	s_add_u32 s100, s100, s89
	s_addc_u32 s101, s101, 0
	global_load_dword v96, v178, s[100:101] nt
	s_add_u32 s100, s100, s89
	s_addc_u32 s101, s101, 0
	global_load_dword v97, v178, s[100:101] nt
	s_add_u32 s100, s100, s89
	s_addc_u32 s101, s101, 0
	s_waitcnt vmcnt(16)
	v_mul_f32_e32 v66, 0x42000000, v66
	v_mul_f32_e32 v67, 0x42000000, v67
	v_mul_f32_e32 v68, 0x42000000, v68
	v_mul_f32_e32 v69, 0x42000000, v69
	v_mul_f32_e32 v70, 0x42000000, v70
	v_mul_f32_e32 v71, 0x42000000, v71
	v_mul_f32_e32 v72, 0x42000000, v72
	v_mul_f32_e32 v73, 0x42000000, v73
	v_mul_f32_e32 v74, 0x42000000, v74
	v_mul_f32_e32 v75, 0x42000000, v75
	v_mul_f32_e32 v76, 0x42000000, v76
	v_mul_f32_e32 v77, 0x42000000, v77
	v_mul_f32_e32 v78, 0x42000000, v78
	v_mul_f32_e32 v79, 0x42000000, v79
	v_mul_f32_e32 v80, 0x42000000, v80
	v_mul_f32_e32 v81, 0x42000000, v81
	v_cvt_pk_fp8_f32 v162, v66, v67
	v_cvt_pk_fp8_f32 v163, v70, v71
	v_cvt_pk_fp8_f32 v164, v74, v75
	v_cvt_pk_fp8_f32 v165, v78, v79
	v_cvt_pk_fp8_f32 v162, v68, v69 op_sel:[0,0,1]
	v_cvt_pk_fp8_f32 v163, v72, v73 op_sel:[0,0,1]
	v_cvt_pk_fp8_f32 v164, v76, v77 op_sel:[0,0,1]
	v_cvt_pk_fp8_f32 v165, v80, v81 op_sel:[0,0,1]
	s_waitcnt vmcnt(0)
	v_mul_f32_e32 v82, 0x42000000, v82
	v_mul_f32_e32 v83, 0x42000000, v83
	v_mul_f32_e32 v84, 0x42000000, v84
	v_mul_f32_e32 v85, 0x42000000, v85
	v_mul_f32_e32 v86, 0x42000000, v86
	v_mul_f32_e32 v87, 0x42000000, v87
	v_mul_f32_e32 v88, 0x42000000, v88
	v_mul_f32_e32 v89, 0x42000000, v89
	v_mul_f32_e32 v90, 0x42000000, v90
	v_mul_f32_e32 v91, 0x42000000, v91
	v_mul_f32_e32 v92, 0x42000000, v92
	v_mul_f32_e32 v93, 0x42000000, v93
	v_mul_f32_e32 v94, 0x42000000, v94
	v_mul_f32_e32 v95, 0x42000000, v95
	v_mul_f32_e32 v96, 0x42000000, v96
	v_mul_f32_e32 v97, 0x42000000, v97
	v_cvt_pk_fp8_f32 v166, v82, v83
	v_cvt_pk_fp8_f32 v167, v86, v87
	v_cvt_pk_fp8_f32 v168, v90, v91
	v_cvt_pk_fp8_f32 v169, v94, v95
	v_cvt_pk_fp8_f32 v166, v84, v85 op_sel:[0,0,1]
	v_cvt_pk_fp8_f32 v167, v88, v89 op_sel:[0,0,1]
	v_cvt_pk_fp8_f32 v168, v92, v93 op_sel:[0,0,1]
	v_cvt_pk_fp8_f32 v169, v96, v97 op_sel:[0,0,1]
	s_mov_b32 vcc_lo, 0xaaaaaaaa
	s_mov_b32 vcc_hi, 0xaaaaaaaa
	s_nop 1
	v_cndmask_b32_dpp v170, v154, v158, vcc quad_perm:[1,0,3,2] row_mask:0xf bank_mask:0xf
	v_cndmask_b32_dpp v174, v162, v166, vcc quad_perm:[1,0,3,2] row_mask:0xf bank_mask:0xf
	v_cndmask_b32_dpp v171, v155, v159, vcc quad_perm:[1,0,3,2] row_mask:0xf bank_mask:0xf
	v_cndmask_b32_dpp v175, v163, v167, vcc quad_perm:[1,0,3,2] row_mask:0xf bank_mask:0xf
	v_cndmask_b32_dpp v172, v156, v160, vcc quad_perm:[1,0,3,2] row_mask:0xf bank_mask:0xf
	v_cndmask_b32_dpp v176, v164, v168, vcc quad_perm:[1,0,3,2] row_mask:0xf bank_mask:0xf
	v_cndmask_b32_dpp v173, v157, v161, vcc quad_perm:[1,0,3,2] row_mask:0xf bank_mask:0xf
	v_cndmask_b32_dpp v177, v165, v169, vcc quad_perm:[1,0,3,2] row_mask:0xf bank_mask:0xf
	s_mov_b32 vcc_lo, 0x55555555
	s_mov_b32 vcc_hi, 0x55555555
	s_nop 1
	v_cndmask_b32_dpp v154, v158, v154, vcc quad_perm:[1,0,3,2] row_mask:0xf bank_mask:0xf
	v_cndmask_b32_dpp v162, v166, v162, vcc quad_perm:[1,0,3,2] row_mask:0xf bank_mask:0xf
	v_cndmask_b32_dpp v155, v159, v155, vcc quad_perm:[1,0,3,2] row_mask:0xf bank_mask:0xf
	v_cndmask_b32_dpp v163, v167, v163, vcc quad_perm:[1,0,3,2] row_mask:0xf bank_mask:0xf
	v_cndmask_b32_dpp v156, v160, v156, vcc quad_perm:[1,0,3,2] row_mask:0xf bank_mask:0xf
	v_cndmask_b32_dpp v164, v168, v164, vcc quad_perm:[1,0,3,2] row_mask:0xf bank_mask:0xf
	v_cndmask_b32_dpp v157, v161, v157, vcc quad_perm:[1,0,3,2] row_mask:0xf bank_mask:0xf
	v_cndmask_b32_dpp v165, v169, v165, vcc quad_perm:[1,0,3,2] row_mask:0xf bank_mask:0xf
	s_mov_b32 vcc_lo, 0xcccccccc
	s_mov_b32 vcc_hi, 0xcccccccc
	s_nop 1
	v_cndmask_b32_dpp v158, v154, v162, vcc quad_perm:[2,3,0,1] row_mask:0xf bank_mask:0xf
	v_cndmask_b32_dpp v166, v170, v174, vcc quad_perm:[2,3,0,1] row_mask:0xf bank_mask:0xf
	v_cndmask_b32_dpp v159, v155, v163, vcc quad_perm:[2,3,0,1] row_mask:0xf bank_mask:0xf
	v_cndmask_b32_dpp v167, v171, v175, vcc quad_perm:[2,3,0,1] row_mask:0xf bank_mask:0xf
	v_cndmask_b32_dpp v160, v156, v164, vcc quad_perm:[2,3,0,1] row_mask:0xf bank_mask:0xf
	v_cndmask_b32_dpp v168, v172, v176, vcc quad_perm:[2,3,0,1] row_mask:0xf bank_mask:0xf
	v_cndmask_b32_dpp v161, v157, v165, vcc quad_perm:[2,3,0,1] row_mask:0xf bank_mask:0xf
	v_cndmask_b32_dpp v169, v173, v177, vcc quad_perm:[2,3,0,1] row_mask:0xf bank_mask:0xf
	s_mov_b32 vcc_lo, 0x33333333
	s_mov_b32 vcc_hi, 0x33333333
	s_nop 1
	v_cndmask_b32_dpp v154, v162, v154, vcc quad_perm:[2,3,0,1] row_mask:0xf bank_mask:0xf
	v_cndmask_b32_dpp v170, v174, v170, vcc quad_perm:[2,3,0,1] row_mask:0xf bank_mask:0xf
	v_cndmask_b32_dpp v155, v163, v155, vcc quad_perm:[2,3,0,1] row_mask:0xf bank_mask:0xf
	v_cndmask_b32_dpp v171, v175, v171, vcc quad_perm:[2,3,0,1] row_mask:0xf bank_mask:0xf
	v_cndmask_b32_dpp v156, v164, v156, vcc quad_perm:[2,3,0,1] row_mask:0xf bank_mask:0xf
	v_cndmask_b32_dpp v172, v176, v172, vcc quad_perm:[2,3,0,1] row_mask:0xf bank_mask:0xf
	v_cndmask_b32_dpp v157, v165, v157, vcc quad_perm:[2,3,0,1] row_mask:0xf bank_mask:0xf
	v_cndmask_b32_dpp v173, v177, v173, vcc quad_perm:[2,3,0,1] row_mask:0xf bank_mask:0xf
	global_store_dwordx4 v179, v[154:157], s[82:83] nt
	global_store_dwordx4 v180, v[170:173], s[82:83] nt
	global_store_dwordx4 v181, v[158:161], s[82:83] nt
	global_store_dwordx4 v190, v[166:169], s[82:83] nt
	v_readlane_b32 s2, v239, 0
	s_lshr_b32 s2, s2, 6
	s_add_i32 s2, s2, 6
	s_cmp_gt_u32 s2, 13
	s_cbranch_scc1 .Lhw_seam4_done
	s_add_i32 s2, s2, 56
	s_mul_i32 s2, s2, s74
	v_readlane_b32 s9, v239, 23
	s_lshr_b32 s9, s9, 3
	s_add_i32 s2, s2, s9
	s_cmp_gt_u32 s2, 24575
	s_cbranch_scc1 .Lhw_seam4_done
	v_mbcnt_lo_u32_b32 v178, -1, 0
	v_mbcnt_hi_u32_b32 v178, -1, v178
	v_and_b32_e32 v179, 60, v178
	v_lshlrev_b32_e32 v179, 10, v179
	v_and_b32_e32 v180, 3, v178
	v_lshl_or_b32 v179, v180, 4, v179
	v_add_u32_e32 v180, 0x400, v179
	v_add_u32_e32 v181, 0x800, v179
	v_add_u32_e32 v190, 0xc00, v179
	v_lshlrev_b32_e32 v178, 2, v178
	s_cmp_lt_u32 s2, 16384
	s_cbranch_scc0 .Lhw_dn_s4_1
	s_lshr_b32 s9, s2, 9
	s_bfe_u32 s32, s2, 0x40005
	s_and_b32 s53, s2, 31
	s_lshl_b32 s69, s9, 23
	s_lshl_b32 s100, s32, 19
	s_add_i32 s69, s69, s100
	s_lshl_b32 s100, s53, 8
	s_add_i32 s69, s69, s100
	s_lshl_b32 s98, s9, 11
	s_bfe_u32 s100, s53, 0x30001
	s_lshl_b32 s100, s100, 8
	s_add_i32 s98, s98, s100
	s_lshr_b32 s100, s53, 4
	s_lshl_b32 s100, s100, 7
	s_add_i32 s98, s98, s100
	s_and_b32 s100, s53, 1
	s_lshl_b32 s100, s100, 6
	s_add_i32 s98, s98, s100
	s_lshl_b32 s98, s98, 10
	s_lshl_b32 s100, s32, 6
	s_add_i32 s98, s98, s100
	s_add_i32 s98, s98, 0x2000000
	v_readlane_b32 s82, v239, 11
	v_readlane_b32 s83, v239, 12
	s_movk_i32 s89, 8192
	s_branch .Lhw_go_s4_1

.Lhw_go_s5_0:
	s_add_u32 s100, s82, s69
	s_addc_u32 s101, s83, 0
	v_readlane_b32 s82, v239, 44
	v_readlane_b32 s83, v239, 45
	s_add_u32 s82, s82, s98
	s_addc_u32 s83, s83, 0
	global_load_dword v34, v178, s[100:101] nt
	s_add_u32 s100, s100, s89
	s_addc_u32 s101, s101, 0
	global_load_dword v35, v178, s[100:101] nt
	s_add_u32 s100, s100, s89
	s_addc_u32 s101, s101, 0
	global_load_dword v36, v178, s[100:101] nt
	s_add_u32 s100, s100, s89
	s_addc_u32 s101, s101, 0
	global_load_dword v37, v178, s[100:101] nt
	s_add_u32 s100, s100, s89
	s_addc_u32 s101, s101, 0
	global_load_dword v38, v178, s[100:101] nt
	s_add_u32 s100, s100, s89
	s_addc_u32 s101, s101, 0
	global_load_dword v39, v178, s[100:101] nt
	s_add_u32 s100, s100, s89
	s_addc_u32 s101, s101, 0
	global_load_dword v40, v178, s[100:101] nt
	s_add_u32 s100, s100, s89
	s_addc_u32 s101, s101, 0
	global_load_dword v41, v178, s[100:101] nt
	s_add_u32 s100, s100, s89
	s_addc_u32 s101, s101, 0
	global_load_dword v42, v178, s[100:101] nt
	s_add_u32 s100, s100, s89
	s_addc_u32 s101, s101, 0
	global_load_dword v43, v178, s[100:101] nt
	s_add_u32 s100, s100, s89
	s_addc_u32 s101, s101, 0
	global_load_dword v44, v178, s[100:101] nt
	s_add_u32 s100, s100, s89
	s_addc_u32 s101, s101, 0
	global_load_dword v45, v178, s[100:101] nt
	s_add_u32 s100, s100, s89
	s_addc_u32 s101, s101, 0
	global_load_dword v46, v178, s[100:101] nt
	s_add_u32 s100, s100, s89
	s_addc_u32 s101, s101, 0
	global_load_dword v47, v178, s[100:101] nt
	s_add_u32 s100, s100, s89
	s_addc_u32 s101, s101, 0
	global_load_dword v48, v178, s[100:101] nt
	s_add_u32 s100, s100, s89
	s_addc_u32 s101, s101, 0
	global_load_dword v49, v178, s[100:101] nt
	s_add_u32 s100, s100, s89
	s_addc_u32 s101, s101, 0
	global_load_dword v50, v178, s[100:101] nt
	s_add_u32 s100, s100, s89
	s_addc_u32 s101, s101, 0
	global_load_dword v51, v178, s[100:101] nt
	s_add_u32 s100, s100, s89
	s_addc_u32 s101, s101, 0
	global_load_dword v52, v178, s[100:101] nt
	s_add_u32 s100, s100, s89
	s_addc_u32 s101, s101, 0
	global_load_dword v53, v178, s[100:101] nt
	s_add_u32 s100, s100, s89
	s_addc_u32 s101, s101, 0
	global_load_dword v54, v178, s[100:101] nt
	s_add_u32 s100, s100, s89
	s_addc_u32 s101, s101, 0
	global_load_dword v55, v178, s[100:101] nt
	s_add_u32 s100, s100, s89
	s_addc_u32 s101, s101, 0
	global_load_dword v56, v178, s[100:101] nt
	s_add_u32 s100, s100, s89
	s_addc_u32 s101, s101, 0
	global_load_dword v57, v178, s[100:101] nt
	s_add_u32 s100, s100, s89
	s_addc_u32 s101, s101, 0
	global_load_dword v58, v178, s[100:101] nt
	s_add_u32 s100, s100, s89
	s_addc_u32 s101, s101, 0
	global_load_dword v59, v178, s[100:101] nt
	s_add_u32 s100, s100, s89
	s_addc_u32 s101, s101, 0
	global_load_dword v60, v178, s[100:101] nt
	s_add_u32 s100, s100, s89
	s_addc_u32 s101, s101, 0
	global_load_dword v61, v178, s[100:101] nt
	s_add_u32 s100, s100, s89
	s_addc_u32 s101, s101, 0
	global_load_dword v62, v178, s[100:101] nt
	s_add_u32 s100, s100, s89
	s_addc_u32 s101, s101, 0
	global_load_dword v63, v178, s[100:101] nt
	s_add_u32 s100, s100, s89
	s_addc_u32 s101, s101, 0
	global_load_dword v64, v178, s[100:101] nt
	s_add_u32 s100, s100, s89
	s_addc_u32 s101, s101, 0
	global_load_dword v65, v178, s[100:101] nt
	s_add_u32 s100, s100, s89
	s_addc_u32 s101, s101, 0
	s_waitcnt vmcnt(16)
	v_mul_f32_e32 v34, 0x42000000, v34
	v_mul_f32_e32 v35, 0x42000000, v35
	v_mul_f32_e32 v36, 0x42000000, v36
	v_mul_f32_e32 v37, 0x42000000, v37
	v_mul_f32_e32 v38, 0x42000000, v38
	v_mul_f32_e32 v39, 0x42000000, v39
	v_mul_f32_e32 v40, 0x42000000, v40
	v_mul_f32_e32 v41, 0x42000000, v41
	v_mul_f32_e32 v42, 0x42000000, v42
	v_mul_f32_e32 v43, 0x42000000, v43
	v_mul_f32_e32 v44, 0x42000000, v44
	v_mul_f32_e32 v45, 0x42000000, v45
	v_mul_f32_e32 v46, 0x42000000, v46
	v_mul_f32_e32 v47, 0x42000000, v47
	v_mul_f32_e32 v48, 0x42000000, v48
	v_mul_f32_e32 v49, 0x42000000, v49
	v_cvt_pk_fp8_f32 v154, v34, v35
	v_cvt_pk_fp8_f32 v155, v38, v39
	v_cvt_pk_fp8_f32 v156, v42, v43
	v_cvt_pk_fp8_f32 v157, v46, v47
	v_cvt_pk_fp8_f32 v154, v36, v37 op_sel:[0,0,1]
	v_cvt_pk_fp8_f32 v155, v40, v41 op_sel:[0,0,1]
	v_cvt_pk_fp8_f32 v156, v44, v45 op_sel:[0,0,1]
	v_cvt_pk_fp8_f32 v157, v48, v49 op_sel:[0,0,1]
	global_load_dword v66, v178, s[100:101] nt
	s_add_u32 s100, s100, s89
	s_addc_u32 s101, s101, 0
	global_load_dword v67, v178, s[100:101] nt
	s_add_u32 s100, s100, s89
	s_addc_u32 s101, s101, 0
	global_load_dword v68, v178, s[100:101] nt
	s_add_u32 s100, s100, s89
	s_addc_u32 s101, s101, 0
	global_load_dword v69, v178, s[100:101] nt
	s_add_u32 s100, s100, s89
	s_addc_u32 s101, s101, 0
	global_load_dword v70, v178, s[100:101] nt
	s_add_u32 s100, s100, s89
	s_addc_u32 s101, s101, 0
	global_load_dword v71, v178, s[100:101] nt
	s_add_u32 s100, s100, s89
	s_addc_u32 s101, s101, 0
	global_load_dword v72, v178, s[100:101] nt
	s_add_u32 s100, s100, s89
	s_addc_u32 s101, s101, 0
	global_load_dword v73, v178, s[100:101] nt
	s_add_u32 s100, s100, s89
	s_addc_u32 s101, s101, 0
	global_load_dword v74, v178, s[100:101] nt
	s_add_u32 s100, s100, s89
	s_addc_u32 s101, s101, 0
	global_load_dword v75, v178, s[100:101] nt
	s_add_u32 s100, s100, s89
	s_addc_u32 s101, s101, 0
	global_load_dword v76, v178, s[100:101] nt
	s_add_u32 s100, s100, s89
	s_addc_u32 s101, s101, 0
	global_load_dword v77, v178, s[100:101] nt
	s_add_u32 s100, s100, s89
	s_addc_u32 s101, s101, 0
	global_load_dword v78, v178, s[100:101] nt
	s_add_u32 s100, s100, s89
	s_addc_u32 s101, s101, 0
	global_load_dword v79, v178, s[100:101] nt
	s_add_u32 s100, s100, s89
	s_addc_u32 s101, s101, 0
	global_load_dword v80, v178, s[100:101] nt
	s_add_u32 s100, s100, s89
	s_addc_u32 s101, s101, 0
	global_load_dword v81, v178, s[100:101] nt
	s_add_u32 s100, s100, s89
	s_addc_u32 s101, s101, 0
	s_waitcnt vmcnt(16)
	v_mul_f32_e32 v50, 0x42000000, v50
	v_mul_f32_e32 v51, 0x42000000, v51
	v_mul_f32_e32 v52, 0x42000000, v52
	v_mul_f32_e32 v53, 0x42000000, v53
	v_mul_f32_e32 v54, 0x42000000, v54
	v_mul_f32_e32 v55, 0x42000000, v55
	v_mul_f32_e32 v56, 0x42000000, v56
	v_mul_f32_e32 v57, 0x42000000, v57
	v_mul_f32_e32 v58, 0x42000000, v58
	v_mul_f32_e32 v59, 0x42000000, v59
	v_mul_f32_e32 v60, 0x42000000, v60
	v_mul_f32_e32 v61, 0x42000000, v61
	v_mul_f32_e32 v62, 0x42000000, v62
	v_mul_f32_e32 v63, 0x42000000, v63
	v_mul_f32_e32 v64, 0x42000000, v64
	v_mul_f32_e32 v65, 0x42000000, v65
	v_cvt_pk_fp8_f32 v158, v50, v51
	v_cvt_pk_fp8_f32 v159, v54, v55
	v_cvt_pk_fp8_f32 v160, v58, v59
	v_cvt_pk_fp8_f32 v161, v62, v63
	v_cvt_pk_fp8_f32 v158, v52, v53 op_sel:[0,0,1]
	v_cvt_pk_fp8_f32 v159, v56, v57 op_sel:[0,0,1]
	v_cvt_pk_fp8_f32 v160, v60, v61 op_sel:[0,0,1]
	v_cvt_pk_fp8_f32 v161, v64, v65 op_sel:[0,0,1]
	global_load_dword v82, v178, s[100:101] nt
	s_add_u32 s100, s100, s89
	s_addc_u32 s101, s101, 0
	global_load_dword v83, v178, s[100:101] nt
	s_add_u32 s100, s100, s89
	s_addc_u32 s101, s101, 0
	global_load_dword v84, v178, s[100:101] nt
	s_add_u32 s100, s100, s89
	s_addc_u32 s101, s101, 0
	global_load_dword v85, v178, s[100:101] nt
	s_add_u32 s100, s100, s89
	s_addc_u32 s101, s101, 0
	global_load_dword v86, v178, s[100:101] nt
	s_add_u32 s100, s100, s89
	s_addc_u32 s101, s101, 0
	global_load_dword v87, v178, s[100:101] nt
	s_add_u32 s100, s100, s89
	s_addc_u32 s101, s101, 0
	global_load_dword v88, v178, s[100:101] nt
	s_add_u32 s100, s100, s89
	s_addc_u32 s101, s101, 0
	global_load_dword v89, v178, s[100:101] nt
	s_add_u32 s100, s100, s89
	s_addc_u32 s101, s101, 0
	global_load_dword v90, v178, s[100:101] nt
	s_add_u32 s100, s100, s89
	s_addc_u32 s101, s101, 0
	global_load_dword v91, v178, s[100:101] nt
	s_add_u32 s100, s100, s89
	s_addc_u32 s101, s101, 0
	global_load_dword v92, v178, s[100:101] nt
	s_add_u32 s100, s100, s89
	s_addc_u32 s101, s101, 0
	global_load_dword v93, v178, s[100:101] nt
	s_add_u32 s100, s100, s89
	s_addc_u32 s101, s101, 0
	global_load_dword v94, v178, s[100:101] nt
	s_add_u32 s100, s100, s89
	s_addc_u32 s101, s101, 0
	global_load_dword v95, v178, s[100:101] nt
	s_add_u32 s100, s100, s89
	s_addc_u32 s101, s101, 0
	global_load_dword v96, v178, s[100:101] nt
	s_add_u32 s100, s100, s89
	s_addc_u32 s101, s101, 0
	global_load_dword v97, v178, s[100:101] nt
	s_add_u32 s100, s100, s89
	s_addc_u32 s101, s101, 0
	s_waitcnt vmcnt(16)
	v_mul_f32_e32 v66, 0x42000000, v66
	v_mul_f32_e32 v67, 0x42000000, v67
	v_mul_f32_e32 v68, 0x42000000, v68
	v_mul_f32_e32 v69, 0x42000000, v69
	v_mul_f32_e32 v70, 0x42000000, v70
	v_mul_f32_e32 v71, 0x42000000, v71
	v_mul_f32_e32 v72, 0x42000000, v72
	v_mul_f32_e32 v73, 0x42000000, v73
	v_mul_f32_e32 v74, 0x42000000, v74
	v_mul_f32_e32 v75, 0x42000000, v75
	v_mul_f32_e32 v76, 0x42000000, v76
	v_mul_f32_e32 v77, 0x42000000, v77
	v_mul_f32_e32 v78, 0x42000000, v78
	v_mul_f32_e32 v79, 0x42000000, v79
	v_mul_f32_e32 v80, 0x42000000, v80
	v_mul_f32_e32 v81, 0x42000000, v81
	v_cvt_pk_fp8_f32 v162, v66, v67
	v_cvt_pk_fp8_f32 v163, v70, v71
	v_cvt_pk_fp8_f32 v164, v74, v75
	v_cvt_pk_fp8_f32 v165, v78, v79
	v_cvt_pk_fp8_f32 v162, v68, v69 op_sel:[0,0,1]
	v_cvt_pk_fp8_f32 v163, v72, v73 op_sel:[0,0,1]
	v_cvt_pk_fp8_f32 v164, v76, v77 op_sel:[0,0,1]
	v_cvt_pk_fp8_f32 v165, v80, v81 op_sel:[0,0,1]
	s_waitcnt vmcnt(0)
	v_mul_f32_e32 v82, 0x42000000, v82
	v_mul_f32_e32 v83, 0x42000000, v83
	v_mul_f32_e32 v84, 0x42000000, v84
	v_mul_f32_e32 v85, 0x42000000, v85
	v_mul_f32_e32 v86, 0x42000000, v86
	v_mul_f32_e32 v87, 0x42000000, v87
	v_mul_f32_e32 v88, 0x42000000, v88
	v_mul_f32_e32 v89, 0x42000000, v89
	v_mul_f32_e32 v90, 0x42000000, v90
	v_mul_f32_e32 v91, 0x42000000, v91
	v_mul_f32_e32 v92, 0x42000000, v92
	v_mul_f32_e32 v93, 0x42000000, v93
	v_mul_f32_e32 v94, 0x42000000, v94
	v_mul_f32_e32 v95, 0x42000000, v95
	v_mul_f32_e32 v96, 0x42000000, v96
	v_mul_f32_e32 v97, 0x42000000, v97
	v_cvt_pk_fp8_f32 v166, v82, v83
	v_cvt_pk_fp8_f32 v167, v86, v87
	v_cvt_pk_fp8_f32 v168, v90, v91
	v_cvt_pk_fp8_f32 v169, v94, v95
	v_cvt_pk_fp8_f32 v166, v84, v85 op_sel:[0,0,1]
	v_cvt_pk_fp8_f32 v167, v88, v89 op_sel:[0,0,1]
	v_cvt_pk_fp8_f32 v168, v92, v93 op_sel:[0,0,1]
	v_cvt_pk_fp8_f32 v169, v96, v97 op_sel:[0,0,1]
	s_mov_b32 vcc_lo, 0xaaaaaaaa
	s_mov_b32 vcc_hi, 0xaaaaaaaa
	s_nop 1
	v_cndmask_b32_dpp v170, v154, v158, vcc quad_perm:[1,0,3,2] row_mask:0xf bank_mask:0xf
	v_cndmask_b32_dpp v174, v162, v166, vcc quad_perm:[1,0,3,2] row_mask:0xf bank_mask:0xf
	v_cndmask_b32_dpp v171, v155, v159, vcc quad_perm:[1,0,3,2] row_mask:0xf bank_mask:0xf
	v_cndmask_b32_dpp v175, v163, v167, vcc quad_perm:[1,0,3,2] row_mask:0xf bank_mask:0xf
	v_cndmask_b32_dpp v172, v156, v160, vcc quad_perm:[1,0,3,2] row_mask:0xf bank_mask:0xf
	v_cndmask_b32_dpp v176, v164, v168, vcc quad_perm:[1,0,3,2] row_mask:0xf bank_mask:0xf
	v_cndmask_b32_dpp v173, v157, v161, vcc quad_perm:[1,0,3,2] row_mask:0xf bank_mask:0xf
	v_cndmask_b32_dpp v177, v165, v169, vcc quad_perm:[1,0,3,2] row_mask:0xf bank_mask:0xf
	s_mov_b32 vcc_lo, 0x55555555
	s_mov_b32 vcc_hi, 0x55555555
	s_nop 1
	v_cndmask_b32_dpp v154, v158, v154, vcc quad_perm:[1,0,3,2] row_mask:0xf bank_mask:0xf
	v_cndmask_b32_dpp v162, v166, v162, vcc quad_perm:[1,0,3,2] row_mask:0xf bank_mask:0xf
	v_cndmask_b32_dpp v155, v159, v155, vcc quad_perm:[1,0,3,2] row_mask:0xf bank_mask:0xf
	v_cndmask_b32_dpp v163, v167, v163, vcc quad_perm:[1,0,3,2] row_mask:0xf bank_mask:0xf
	v_cndmask_b32_dpp v156, v160, v156, vcc quad_perm:[1,0,3,2] row_mask:0xf bank_mask:0xf
	v_cndmask_b32_dpp v164, v168, v164, vcc quad_perm:[1,0,3,2] row_mask:0xf bank_mask:0xf
	v_cndmask_b32_dpp v157, v161, v157, vcc quad_perm:[1,0,3,2] row_mask:0xf bank_mask:0xf
	v_cndmask_b32_dpp v165, v169, v165, vcc quad_perm:[1,0,3,2] row_mask:0xf bank_mask:0xf
	s_mov_b32 vcc_lo, 0xcccccccc
	s_mov_b32 vcc_hi, 0xcccccccc
	s_nop 1
	v_cndmask_b32_dpp v158, v154, v162, vcc quad_perm:[2,3,0,1] row_mask:0xf bank_mask:0xf
	v_cndmask_b32_dpp v166, v170, v174, vcc quad_perm:[2,3,0,1] row_mask:0xf bank_mask:0xf
	v_cndmask_b32_dpp v159, v155, v163, vcc quad_perm:[2,3,0,1] row_mask:0xf bank_mask:0xf
	v_cndmask_b32_dpp v167, v171, v175, vcc quad_perm:[2,3,0,1] row_mask:0xf bank_mask:0xf
	v_cndmask_b32_dpp v160, v156, v164, vcc quad_perm:[2,3,0,1] row_mask:0xf bank_mask:0xf
	v_cndmask_b32_dpp v168, v172, v176, vcc quad_perm:[2,3,0,1] row_mask:0xf bank_mask:0xf
	v_cndmask_b32_dpp v161, v157, v165, vcc quad_perm:[2,3,0,1] row_mask:0xf bank_mask:0xf
	v_cndmask_b32_dpp v169, v173, v177, vcc quad_perm:[2,3,0,1] row_mask:0xf bank_mask:0xf
	s_mov_b32 vcc_lo, 0x33333333
	s_mov_b32 vcc_hi, 0x33333333
	s_nop 1
	v_cndmask_b32_dpp v154, v162, v154, vcc quad_perm:[2,3,0,1] row_mask:0xf bank_mask:0xf
	v_cndmask_b32_dpp v170, v174, v170, vcc quad_perm:[2,3,0,1] row_mask:0xf bank_mask:0xf
	v_cndmask_b32_dpp v155, v163, v155, vcc quad_perm:[2,3,0,1] row_mask:0xf bank_mask:0xf
	v_cndmask_b32_dpp v171, v175, v171, vcc quad_perm:[2,3,0,1] row_mask:0xf bank_mask:0xf
	v_cndmask_b32_dpp v156, v164, v156, vcc quad_perm:[2,3,0,1] row_mask:0xf bank_mask:0xf
	v_cndmask_b32_dpp v172, v176, v172, vcc quad_perm:[2,3,0,1] row_mask:0xf bank_mask:0xf
	v_cndmask_b32_dpp v157, v165, v157, vcc quad_perm:[2,3,0,1] row_mask:0xf bank_mask:0xf
	v_cndmask_b32_dpp v173, v177, v173, vcc quad_perm:[2,3,0,1] row_mask:0xf bank_mask:0xf
	global_store_dwordx4 v179, v[154:157], s[82:83] nt
	global_store_dwordx4 v180, v[170:173], s[82:83] nt
	global_store_dwordx4 v181, v[158:161], s[82:83] nt
	global_store_dwordx4 v190, v[166:169], s[82:83] nt
	v_readlane_b32 s2, v239, 0
	s_lshr_b32 s2, s2, 6
	s_add_i32 s2, s2, 6
	s_cmp_gt_u32 s2, 13
	s_cbranch_scc1 .Lhw_seam5_done
	s_add_i32 s2, s2, 70
	s_mul_i32 s2, s2, s74
	v_readlane_b32 s9, v239, 23
	s_lshr_b32 s9, s9, 3
	s_add_i32 s2, s2, s9
	s_cmp_gt_u32 s2, 24575
	s_cbranch_scc1 .Lhw_seam5_done
	v_mbcnt_lo_u32_b32 v178, -1, 0
	v_mbcnt_hi_u32_b32 v178, -1, v178
	v_and_b32_e32 v179, 60, v178
	v_lshlrev_b32_e32 v179, 10, v179
	v_and_b32_e32 v180, 3, v178
	v_lshl_or_b32 v179, v180, 4, v179
	v_add_u32_e32 v180, 0x400, v179
	v_add_u32_e32 v181, 0x800, v179
	v_add_u32_e32 v190, 0xc00, v179
	v_lshlrev_b32_e32 v178, 2, v178
	s_cmp_lt_u32 s2, 16384
	s_cbranch_scc0 .Lhw_dn_s5_1
	s_lshr_b32 s9, s2, 9
	s_bfe_u32 s32, s2, 0x40005
	s_and_b32 s53, s2, 31
	s_lshl_b32 s69, s9, 23
	s_lshl_b32 s100, s32, 19
	s_add_i32 s69, s69, s100
	s_lshl_b32 s100, s53, 8
	s_add_i32 s69, s69, s100
	s_lshl_b32 s98, s9, 11
	s_bfe_u32 s100, s53, 0x30001
	s_lshl_b32 s100, s100, 8
	s_add_i32 s98, s98, s100
	s_lshr_b32 s100, s53, 4
	s_lshl_b32 s100, s100, 7
	s_add_i32 s98, s98, s100
	s_and_b32 s100, s53, 1
	s_lshl_b32 s100, s100, 6
	s_add_i32 s98, s98, s100
	s_lshl_b32 s98, s98, 10
	s_lshl_b32 s100, s32, 6
	s_add_i32 s98, s98, s100
	s_add_i32 s98, s98, 0x2000000
	v_readlane_b32 s82, v239, 11
	v_readlane_b32 s83, v239, 12
	s_movk_i32 s89, 8192
	s_branch .Lhw_go_s5_1

.Lhw_go_s6_0:
	s_add_u32 s100, s82, s69
	s_addc_u32 s101, s83, 0
	v_readlane_b32 s82, v239, 44
	v_readlane_b32 s83, v239, 45
	s_add_u32 s82, s82, s98
	s_addc_u32 s83, s83, 0
	global_load_dword v34, v178, s[100:101] nt
	s_add_u32 s100, s100, s89
	s_addc_u32 s101, s101, 0
	global_load_dword v35, v178, s[100:101] nt
	s_add_u32 s100, s100, s89
	s_addc_u32 s101, s101, 0
	global_load_dword v36, v178, s[100:101] nt
	s_add_u32 s100, s100, s89
	s_addc_u32 s101, s101, 0
	global_load_dword v37, v178, s[100:101] nt
	s_add_u32 s100, s100, s89
	s_addc_u32 s101, s101, 0
	global_load_dword v38, v178, s[100:101] nt
	s_add_u32 s100, s100, s89
	s_addc_u32 s101, s101, 0
	global_load_dword v39, v178, s[100:101] nt
	s_add_u32 s100, s100, s89
	s_addc_u32 s101, s101, 0
	global_load_dword v40, v178, s[100:101] nt
	s_add_u32 s100, s100, s89
	s_addc_u32 s101, s101, 0
	global_load_dword v41, v178, s[100:101] nt
	s_add_u32 s100, s100, s89
	s_addc_u32 s101, s101, 0
	global_load_dword v42, v178, s[100:101] nt
	s_add_u32 s100, s100, s89
	s_addc_u32 s101, s101, 0
	global_load_dword v43, v178, s[100:101] nt
	s_add_u32 s100, s100, s89
	s_addc_u32 s101, s101, 0
	global_load_dword v44, v178, s[100:101] nt
	s_add_u32 s100, s100, s89
	s_addc_u32 s101, s101, 0
	global_load_dword v45, v178, s[100:101] nt
	s_add_u32 s100, s100, s89
	s_addc_u32 s101, s101, 0
	global_load_dword v46, v178, s[100:101] nt
	s_add_u32 s100, s100, s89
	s_addc_u32 s101, s101, 0
	global_load_dword v47, v178, s[100:101] nt
	s_add_u32 s100, s100, s89
	s_addc_u32 s101, s101, 0
	global_load_dword v48, v178, s[100:101] nt
	s_add_u32 s100, s100, s89
	s_addc_u32 s101, s101, 0
	global_load_dword v49, v178, s[100:101] nt
	s_add_u32 s100, s100, s89
	s_addc_u32 s101, s101, 0
	global_load_dword v50, v178, s[100:101] nt
	s_add_u32 s100, s100, s89
	s_addc_u32 s101, s101, 0
	global_load_dword v51, v178, s[100:101] nt
	s_add_u32 s100, s100, s89
	s_addc_u32 s101, s101, 0
	global_load_dword v52, v178, s[100:101] nt
	s_add_u32 s100, s100, s89
	s_addc_u32 s101, s101, 0
	global_load_dword v53, v178, s[100:101] nt
	s_add_u32 s100, s100, s89
	s_addc_u32 s101, s101, 0
	global_load_dword v54, v178, s[100:101] nt
	s_add_u32 s100, s100, s89
	s_addc_u32 s101, s101, 0
	global_load_dword v55, v178, s[100:101] nt
	s_add_u32 s100, s100, s89
	s_addc_u32 s101, s101, 0
	global_load_dword v56, v178, s[100:101] nt
	s_add_u32 s100, s100, s89
	s_addc_u32 s101, s101, 0
	global_load_dword v57, v178, s[100:101] nt
	s_add_u32 s100, s100, s89
	s_addc_u32 s101, s101, 0
	global_load_dword v58, v178, s[100:101] nt
	s_add_u32 s100, s100, s89
	s_addc_u32 s101, s101, 0
	global_load_dword v59, v178, s[100:101] nt
	s_add_u32 s100, s100, s89
	s_addc_u32 s101, s101, 0
	global_load_dword v60, v178, s[100:101] nt
	s_add_u32 s100, s100, s89
	s_addc_u32 s101, s101, 0
	global_load_dword v61, v178, s[100:101] nt
	s_add_u32 s100, s100, s89
	s_addc_u32 s101, s101, 0
	global_load_dword v62, v178, s[100:101] nt
	s_add_u32 s100, s100, s89
	s_addc_u32 s101, s101, 0
	global_load_dword v63, v178, s[100:101] nt
	s_add_u32 s100, s100, s89
	s_addc_u32 s101, s101, 0
	global_load_dword v64, v178, s[100:101] nt
	s_add_u32 s100, s100, s89
	s_addc_u32 s101, s101, 0
	global_load_dword v65, v178, s[100:101] nt
	s_add_u32 s100, s100, s89
	s_addc_u32 s101, s101, 0
	s_waitcnt vmcnt(16)
	v_mul_f32_e32 v34, 0x42000000, v34
	v_mul_f32_e32 v35, 0x42000000, v35
	v_mul_f32_e32 v36, 0x42000000, v36
	v_mul_f32_e32 v37, 0x42000000, v37
	v_mul_f32_e32 v38, 0x42000000, v38
	v_mul_f32_e32 v39, 0x42000000, v39
	v_mul_f32_e32 v40, 0x42000000, v40
	v_mul_f32_e32 v41, 0x42000000, v41
	v_mul_f32_e32 v42, 0x42000000, v42
	v_mul_f32_e32 v43, 0x42000000, v43
	v_mul_f32_e32 v44, 0x42000000, v44
	v_mul_f32_e32 v45, 0x42000000, v45
	v_mul_f32_e32 v46, 0x42000000, v46
	v_mul_f32_e32 v47, 0x42000000, v47
	v_mul_f32_e32 v48, 0x42000000, v48
	v_mul_f32_e32 v49, 0x42000000, v49
	v_cvt_pk_fp8_f32 v154, v34, v35
	v_cvt_pk_fp8_f32 v155, v38, v39
	v_cvt_pk_fp8_f32 v156, v42, v43
	v_cvt_pk_fp8_f32 v157, v46, v47
	v_cvt_pk_fp8_f32 v154, v36, v37 op_sel:[0,0,1]
	v_cvt_pk_fp8_f32 v155, v40, v41 op_sel:[0,0,1]
	v_cvt_pk_fp8_f32 v156, v44, v45 op_sel:[0,0,1]
	v_cvt_pk_fp8_f32 v157, v48, v49 op_sel:[0,0,1]
	global_load_dword v66, v178, s[100:101] nt
	s_add_u32 s100, s100, s89
	s_addc_u32 s101, s101, 0
	global_load_dword v67, v178, s[100:101] nt
	s_add_u32 s100, s100, s89
	s_addc_u32 s101, s101, 0
	global_load_dword v68, v178, s[100:101] nt
	s_add_u32 s100, s100, s89
	s_addc_u32 s101, s101, 0
	global_load_dword v69, v178, s[100:101] nt
	s_add_u32 s100, s100, s89
	s_addc_u32 s101, s101, 0
	global_load_dword v70, v178, s[100:101] nt
	s_add_u32 s100, s100, s89
	s_addc_u32 s101, s101, 0
	global_load_dword v71, v178, s[100:101] nt
	s_add_u32 s100, s100, s89
	s_addc_u32 s101, s101, 0
	global_load_dword v72, v178, s[100:101] nt
	s_add_u32 s100, s100, s89
	s_addc_u32 s101, s101, 0
	global_load_dword v73, v178, s[100:101] nt
	s_add_u32 s100, s100, s89
	s_addc_u32 s101, s101, 0
	global_load_dword v74, v178, s[100:101] nt
	s_add_u32 s100, s100, s89
	s_addc_u32 s101, s101, 0
	global_load_dword v75, v178, s[100:101] nt
	s_add_u32 s100, s100, s89
	s_addc_u32 s101, s101, 0
	global_load_dword v76, v178, s[100:101] nt
	s_add_u32 s100, s100, s89
	s_addc_u32 s101, s101, 0
	global_load_dword v77, v178, s[100:101] nt
	s_add_u32 s100, s100, s89
	s_addc_u32 s101, s101, 0
	global_load_dword v78, v178, s[100:101] nt
	s_add_u32 s100, s100, s89
	s_addc_u32 s101, s101, 0
	global_load_dword v79, v178, s[100:101] nt
	s_add_u32 s100, s100, s89
	s_addc_u32 s101, s101, 0
	global_load_dword v80, v178, s[100:101] nt
	s_add_u32 s100, s100, s89
	s_addc_u32 s101, s101, 0
	global_load_dword v81, v178, s[100:101] nt
	s_add_u32 s100, s100, s89
	s_addc_u32 s101, s101, 0
	s_waitcnt vmcnt(16)
	v_mul_f32_e32 v50, 0x42000000, v50
	v_mul_f32_e32 v51, 0x42000000, v51
	v_mul_f32_e32 v52, 0x42000000, v52
	v_mul_f32_e32 v53, 0x42000000, v53
	v_mul_f32_e32 v54, 0x42000000, v54
	v_mul_f32_e32 v55, 0x42000000, v55
	v_mul_f32_e32 v56, 0x42000000, v56
	v_mul_f32_e32 v57, 0x42000000, v57
	v_mul_f32_e32 v58, 0x42000000, v58
	v_mul_f32_e32 v59, 0x42000000, v59
	v_mul_f32_e32 v60, 0x42000000, v60
	v_mul_f32_e32 v61, 0x42000000, v61
	v_mul_f32_e32 v62, 0x42000000, v62
	v_mul_f32_e32 v63, 0x42000000, v63
	v_mul_f32_e32 v64, 0x42000000, v64
	v_mul_f32_e32 v65, 0x42000000, v65
	v_cvt_pk_fp8_f32 v158, v50, v51
	v_cvt_pk_fp8_f32 v159, v54, v55
	v_cvt_pk_fp8_f32 v160, v58, v59
	v_cvt_pk_fp8_f32 v161, v62, v63
	v_cvt_pk_fp8_f32 v158, v52, v53 op_sel:[0,0,1]
	v_cvt_pk_fp8_f32 v159, v56, v57 op_sel:[0,0,1]
	v_cvt_pk_fp8_f32 v160, v60, v61 op_sel:[0,0,1]
	v_cvt_pk_fp8_f32 v161, v64, v65 op_sel:[0,0,1]
	global_load_dword v82, v178, s[100:101] nt
	s_add_u32 s100, s100, s89
	s_addc_u32 s101, s101, 0
	global_load_dword v83, v178, s[100:101] nt
	s_add_u32 s100, s100, s89
	s_addc_u32 s101, s101, 0
	global_load_dword v84, v178, s[100:101] nt
	s_add_u32 s100, s100, s89
	s_addc_u32 s101, s101, 0
	global_load_dword v85, v178, s[100:101] nt
	s_add_u32 s100, s100, s89
	s_addc_u32 s101, s101, 0
	global_load_dword v86, v178, s[100:101] nt
	s_add_u32 s100, s100, s89
	s_addc_u32 s101, s101, 0
	global_load_dword v87, v178, s[100:101] nt
	s_add_u32 s100, s100, s89
	s_addc_u32 s101, s101, 0
	global_load_dword v88, v178, s[100:101] nt
	s_add_u32 s100, s100, s89
	s_addc_u32 s101, s101, 0
	global_load_dword v89, v178, s[100:101] nt
	s_add_u32 s100, s100, s89
	s_addc_u32 s101, s101, 0
	global_load_dword v90, v178, s[100:101] nt
	s_add_u32 s100, s100, s89
	s_addc_u32 s101, s101, 0
	global_load_dword v91, v178, s[100:101] nt
	s_add_u32 s100, s100, s89
	s_addc_u32 s101, s101, 0
	global_load_dword v92, v178, s[100:101] nt
	s_add_u32 s100, s100, s89
	s_addc_u32 s101, s101, 0
	global_load_dword v93, v178, s[100:101] nt
	s_add_u32 s100, s100, s89
	s_addc_u32 s101, s101, 0
	global_load_dword v94, v178, s[100:101] nt
	s_add_u32 s100, s100, s89
	s_addc_u32 s101, s101, 0
	global_load_dword v95, v178, s[100:101] nt
	s_add_u32 s100, s100, s89
	s_addc_u32 s101, s101, 0
	global_load_dword v96, v178, s[100:101] nt
	s_add_u32 s100, s100, s89
	s_addc_u32 s101, s101, 0
	global_load_dword v97, v178, s[100:101] nt
	s_add_u32 s100, s100, s89
	s_addc_u32 s101, s101, 0
	s_waitcnt vmcnt(16)
	v_mul_f32_e32 v66, 0x42000000, v66
	v_mul_f32_e32 v67, 0x42000000, v67
	v_mul_f32_e32 v68, 0x42000000, v68
	v_mul_f32_e32 v69, 0x42000000, v69
	v_mul_f32_e32 v70, 0x42000000, v70
	v_mul_f32_e32 v71, 0x42000000, v71
	v_mul_f32_e32 v72, 0x42000000, v72
	v_mul_f32_e32 v73, 0x42000000, v73
	v_mul_f32_e32 v74, 0x42000000, v74
	v_mul_f32_e32 v75, 0x42000000, v75
	v_mul_f32_e32 v76, 0x42000000, v76
	v_mul_f32_e32 v77, 0x42000000, v77
	v_mul_f32_e32 v78, 0x42000000, v78
	v_mul_f32_e32 v79, 0x42000000, v79
	v_mul_f32_e32 v80, 0x42000000, v80
	v_mul_f32_e32 v81, 0x42000000, v81
	v_cvt_pk_fp8_f32 v162, v66, v67
	v_cvt_pk_fp8_f32 v163, v70, v71
	v_cvt_pk_fp8_f32 v164, v74, v75
	v_cvt_pk_fp8_f32 v165, v78, v79
	v_cvt_pk_fp8_f32 v162, v68, v69 op_sel:[0,0,1]
	v_cvt_pk_fp8_f32 v163, v72, v73 op_sel:[0,0,1]
	v_cvt_pk_fp8_f32 v164, v76, v77 op_sel:[0,0,1]
	v_cvt_pk_fp8_f32 v165, v80, v81 op_sel:[0,0,1]
	s_waitcnt vmcnt(0)
	v_mul_f32_e32 v82, 0x42000000, v82
	v_mul_f32_e32 v83, 0x42000000, v83
	v_mul_f32_e32 v84, 0x42000000, v84
	v_mul_f32_e32 v85, 0x42000000, v85
	v_mul_f32_e32 v86, 0x42000000, v86
	v_mul_f32_e32 v87, 0x42000000, v87
	v_mul_f32_e32 v88, 0x42000000, v88
	v_mul_f32_e32 v89, 0x42000000, v89
	v_mul_f32_e32 v90, 0x42000000, v90
	v_mul_f32_e32 v91, 0x42000000, v91
	v_mul_f32_e32 v92, 0x42000000, v92
	v_mul_f32_e32 v93, 0x42000000, v93
	v_mul_f32_e32 v94, 0x42000000, v94
	v_mul_f32_e32 v95, 0x42000000, v95
	v_mul_f32_e32 v96, 0x42000000, v96
	v_mul_f32_e32 v97, 0x42000000, v97
	v_cvt_pk_fp8_f32 v166, v82, v83
	v_cvt_pk_fp8_f32 v167, v86, v87
	v_cvt_pk_fp8_f32 v168, v90, v91
	v_cvt_pk_fp8_f32 v169, v94, v95
	v_cvt_pk_fp8_f32 v166, v84, v85 op_sel:[0,0,1]
	v_cvt_pk_fp8_f32 v167, v88, v89 op_sel:[0,0,1]
	v_cvt_pk_fp8_f32 v168, v92, v93 op_sel:[0,0,1]
	v_cvt_pk_fp8_f32 v169, v96, v97 op_sel:[0,0,1]
	s_mov_b32 vcc_lo, 0xaaaaaaaa
	s_mov_b32 vcc_hi, 0xaaaaaaaa
	s_nop 1
	v_cndmask_b32_dpp v170, v154, v158, vcc quad_perm:[1,0,3,2] row_mask:0xf bank_mask:0xf
	v_cndmask_b32_dpp v174, v162, v166, vcc quad_perm:[1,0,3,2] row_mask:0xf bank_mask:0xf
	v_cndmask_b32_dpp v171, v155, v159, vcc quad_perm:[1,0,3,2] row_mask:0xf bank_mask:0xf
	v_cndmask_b32_dpp v175, v163, v167, vcc quad_perm:[1,0,3,2] row_mask:0xf bank_mask:0xf
	v_cndmask_b32_dpp v172, v156, v160, vcc quad_perm:[1,0,3,2] row_mask:0xf bank_mask:0xf
	v_cndmask_b32_dpp v176, v164, v168, vcc quad_perm:[1,0,3,2] row_mask:0xf bank_mask:0xf
	v_cndmask_b32_dpp v173, v157, v161, vcc quad_perm:[1,0,3,2] row_mask:0xf bank_mask:0xf
	v_cndmask_b32_dpp v177, v165, v169, vcc quad_perm:[1,0,3,2] row_mask:0xf bank_mask:0xf
	s_mov_b32 vcc_lo, 0x55555555
	s_mov_b32 vcc_hi, 0x55555555
	s_nop 1
	v_cndmask_b32_dpp v154, v158, v154, vcc quad_perm:[1,0,3,2] row_mask:0xf bank_mask:0xf
	v_cndmask_b32_dpp v162, v166, v162, vcc quad_perm:[1,0,3,2] row_mask:0xf bank_mask:0xf
	v_cndmask_b32_dpp v155, v159, v155, vcc quad_perm:[1,0,3,2] row_mask:0xf bank_mask:0xf
	v_cndmask_b32_dpp v163, v167, v163, vcc quad_perm:[1,0,3,2] row_mask:0xf bank_mask:0xf
	v_cndmask_b32_dpp v156, v160, v156, vcc quad_perm:[1,0,3,2] row_mask:0xf bank_mask:0xf
	v_cndmask_b32_dpp v164, v168, v164, vcc quad_perm:[1,0,3,2] row_mask:0xf bank_mask:0xf
	v_cndmask_b32_dpp v157, v161, v157, vcc quad_perm:[1,0,3,2] row_mask:0xf bank_mask:0xf
	v_cndmask_b32_dpp v165, v169, v165, vcc quad_perm:[1,0,3,2] row_mask:0xf bank_mask:0xf
	s_mov_b32 vcc_lo, 0xcccccccc
	s_mov_b32 vcc_hi, 0xcccccccc
	s_nop 1
	v_cndmask_b32_dpp v158, v154, v162, vcc quad_perm:[2,3,0,1] row_mask:0xf bank_mask:0xf
	v_cndmask_b32_dpp v166, v170, v174, vcc quad_perm:[2,3,0,1] row_mask:0xf bank_mask:0xf
	v_cndmask_b32_dpp v159, v155, v163, vcc quad_perm:[2,3,0,1] row_mask:0xf bank_mask:0xf
	v_cndmask_b32_dpp v167, v171, v175, vcc quad_perm:[2,3,0,1] row_mask:0xf bank_mask:0xf
	v_cndmask_b32_dpp v160, v156, v164, vcc quad_perm:[2,3,0,1] row_mask:0xf bank_mask:0xf
	v_cndmask_b32_dpp v168, v172, v176, vcc quad_perm:[2,3,0,1] row_mask:0xf bank_mask:0xf
	v_cndmask_b32_dpp v161, v157, v165, vcc quad_perm:[2,3,0,1] row_mask:0xf bank_mask:0xf
	v_cndmask_b32_dpp v169, v173, v177, vcc quad_perm:[2,3,0,1] row_mask:0xf bank_mask:0xf
	s_mov_b32 vcc_lo, 0x33333333
	s_mov_b32 vcc_hi, 0x33333333
	s_nop 1
	v_cndmask_b32_dpp v154, v162, v154, vcc quad_perm:[2,3,0,1] row_mask:0xf bank_mask:0xf
	v_cndmask_b32_dpp v170, v174, v170, vcc quad_perm:[2,3,0,1] row_mask:0xf bank_mask:0xf
	v_cndmask_b32_dpp v155, v163, v155, vcc quad_perm:[2,3,0,1] row_mask:0xf bank_mask:0xf
	v_cndmask_b32_dpp v171, v175, v171, vcc quad_perm:[2,3,0,1] row_mask:0xf bank_mask:0xf
	v_cndmask_b32_dpp v156, v164, v156, vcc quad_perm:[2,3,0,1] row_mask:0xf bank_mask:0xf
	v_cndmask_b32_dpp v172, v176, v172, vcc quad_perm:[2,3,0,1] row_mask:0xf bank_mask:0xf
	v_cndmask_b32_dpp v157, v165, v157, vcc quad_perm:[2,3,0,1] row_mask:0xf bank_mask:0xf
	v_cndmask_b32_dpp v173, v177, v173, vcc quad_perm:[2,3,0,1] row_mask:0xf bank_mask:0xf
	global_store_dwordx4 v179, v[154:157], s[82:83] nt
	global_store_dwordx4 v180, v[170:173], s[82:83] nt
	global_store_dwordx4 v181, v[158:161], s[82:83] nt
	global_store_dwordx4 v190, v[166:169], s[82:83] nt
	v_readlane_b32 s2, v239, 0
	s_lshr_b32 s2, s2, 6
	s_add_i32 s2, s2, 6
	s_cmp_gt_u32 s2, 11
	s_cbranch_scc1 .Lhw_seam6_done
	s_add_i32 s2, s2, 84
	s_mul_i32 s2, s2, s74
	v_readlane_b32 s9, v239, 23
	s_lshr_b32 s9, s9, 3
	s_add_i32 s2, s2, s9
	s_cmp_gt_u32 s2, 24575
	s_cbranch_scc1 .Lhw_seam6_done
	v_mbcnt_lo_u32_b32 v178, -1, 0
	v_mbcnt_hi_u32_b32 v178, -1, v178
	v_and_b32_e32 v179, 60, v178
	v_lshlrev_b32_e32 v179, 10, v179
	v_and_b32_e32 v180, 3, v178
	v_lshl_or_b32 v179, v180, 4, v179
	v_add_u32_e32 v180, 0x400, v179
	v_add_u32_e32 v181, 0x800, v179
	v_add_u32_e32 v190, 0xc00, v179
	v_lshlrev_b32_e32 v178, 2, v178
	s_cmp_lt_u32 s2, 16384
	s_cbranch_scc0 .Lhw_dn_s6_1
	s_lshr_b32 s9, s2, 9
	s_bfe_u32 s32, s2, 0x40005
	s_and_b32 s53, s2, 31
	s_lshl_b32 s69, s9, 23
	s_lshl_b32 s100, s32, 19
	s_add_i32 s69, s69, s100
	s_lshl_b32 s100, s53, 8
	s_add_i32 s69, s69, s100
	s_lshl_b32 s98, s9, 11
	s_bfe_u32 s100, s53, 0x30001
	s_lshl_b32 s100, s100, 8
	s_add_i32 s98, s98, s100
	s_lshr_b32 s100, s53, 4
	s_lshl_b32 s100, s100, 7
	s_add_i32 s98, s98, s100
	s_and_b32 s100, s53, 1
	s_lshl_b32 s100, s100, 6
	s_add_i32 s98, s98, s100
	s_lshl_b32 s98, s98, 10
	s_lshl_b32 s100, s32, 6
	s_add_i32 s98, s98, s100
	s_add_i32 s98, s98, 0x2000000
	v_readlane_b32 s82, v239, 11
	v_readlane_b32 s83, v239, 12
	s_movk_i32 s89, 8192
	s_branch .Lhw_go_s6_1
